# static s_setprio 1 for waves 4-7 during the ten GEMM phases, per-segment flips removed, on top of the barrier change
# baseline (speedup 1.0000x reference)
; #define MKCTX() Ctx C; { int t_ = tid_from_wave(wave_s); asm volatile("" : "+v"(t_)); C.lds = (LAS unsigned char*)lds_raw; C.tid = t_; C.lane = t_ & 63; C.wave = __builtin_amdgcn_readfirstlane(t_ >> 6); \
;         C.G = gridDim.x; const int bx_ = blockIdx.x; C.vcu = (C.G % 8 == 0) ? (bx_ % 8) * (C.G / 8) + bx_ / 8 : bx_; C.gw = C.vcu * NWAVES + C.wave; C.NGW = C.G * NWAVES; }
; __global__ void __launch_bounds__(NWAVES * 64, 2) fwd(Args args) {
;     ...
;     if (IN(2)) for (int rep_ = 0; rep_ < NREP(2); ++rep_) { MKCTX(); pg8::Gemm g{HN, (const bf16*)(ws + WS_WIN0), NTOK, EVEN_IN, DM / 2}; pg8::StaticOrder S; S.init(NTOK, EVEN_IN, C.G, (int)blockIdx.x);
;         pg8::EpiProj0I E{PROJ, EVEN_IN, QS_EVEN, (const float*)(ws + WS_SA), ctl + CW_CM0}; pg8::gemm_phase<pg8::EpiProj0I, pg8::StaticOrder, true, true, false, true>(C.lds, g, S, E, wave_s);
.LBB0_227:
	s_cmp_lt_i32 s94, 3
	s_cselect_b64 s[0:1], -1, 0
	s_add_u32 s58, s92, 0x9800000
	s_addc_u32 s59, s93, 0
	s_add_u32 s24, s92, 0xd800000
	s_addc_u32 s25, s93, 0
	s_and_b64 s[6:7], s[0:1], s[2:3]
	s_andn2_b64 vcc, exec, s[6:7]
	s_cbranch_vccnz .LBB0_288
	s_cmp_lt_u32 s96, 0x100
	s_cbranch_scc1 .Lsp_2
	s_setprio 1
.Lsp_2:
	v_readlane_b32 s2, v254, 0
	s_waitcnt vmcnt(9)
	v_mbcnt_lo_u32_b32 v0, -1, 0
	v_mbcnt_hi_u32_b32 v0, -1, v0
	v_readlane_b32 s3, v254, 1
	v_add_u32_e32 v178, s96, v0
	s_load_dword s19, s[2:3], 0x120
	s_ashr_i32 s0, s33, 31
	s_lshr_b32 s0, s0, 29
	s_add_i32 s0, s33, s0
	s_ashr_i32 s1, s0, 3
	s_and_b32 s0, s0, -8
	s_sub_i32 s5, s33, s0
	s_waitcnt lgkmcnt(0)
	s_and_b32 s0, s19, 7
	v_readfirstlane_b32 s21, v178
	s_cmp_lg_u32 s0, 0
	s_mov_b32 s23, s33
	s_cbranch_scc1 .LBB0_230
	s_ashr_i32 s0, s19, 3
	s_mul_i32 s0, s0, s5
	s_add_i32 s23, s0, s1

; __device__ __forceinline__ int tid_from_wave(int wave) { unsigned l_; asm volatile("v_mbcnt_lo_u32_b32 %0, -1, 0\n\tv_mbcnt_hi_u32_b32 %0, -1, %0" : "=v"(l_)); return wave * 64 + (int)l_; }
; __device__ __forceinline__ unsigned xb_ld(unsigned* p)              { return __hip_atomic_load(p, __ATOMIC_RELAXED, __HIP_MEMORY_SCOPE_AGENT); }
; __device__ __forceinline__ unsigned xb_add(unsigned* p, unsigned v) { return __hip_atomic_fetch_add(p, v, __ATOMIC_RELAXED, __HIP_MEMORY_SCOPE_AGENT); }
; __device__ __forceinline__ void xcd_barrier_complete(unsigned* bar, unsigned x, unsigned& nloc, unsigned& nx) {
;     const unsigned G = gridDim.x * gridDim.y * gridDim.z;
;     unsigned sum, cnt, mine, sp = 0u;
;     for (;;) {
;         sum = 0u; cnt = 0u; mine = 0u;
; #pragma unroll
;         for (unsigned j = 0; j < 16; ++j) { const unsigned c = xb_ld(&bar[XB_XCNT(j)]); sum += c; cnt += (c > 0u) ? 1u : 0u; mine = (j == x) ? c : mine; }
;         if (sum == G) break;
;         __builtin_amdgcn_s_sleep(1);
;         if ((++sp & 255u) == 0u) { if (xb_ld(&bar[XB_TMO])) break; if (sp > XB_SPIN_CAP) { atomicAdd(&bar[XB_TMO], 1u); break; } }
; __device__ __forceinline__ void xcd_barrier(const XcdBarrier& b) {
;     asm volatile("s_waitcnt vmcnt(0)" ::: "memory");
;     __syncthreads();
;     if (tid_from_wave(b.wave) == 0) {
;         unsigned* bar = b.bar;
;         __builtin_amdgcn_s_waitcnt(0);
;         unsigned nloc = b.st[0], nx = b.st[1];
;         if (nloc == 0u) { xcd_barrier_complete(bar, b.x, nloc, nx); b.st[0] = nloc; b.st[1] = nx; }
;         const unsigned old = xb_add(&bar[XB_XSUB(b.x)], 1u);
.LBB0_288:
	s_setprio 0
	s_cmp_gt_i32 s95, 3
	s_cselect_b64 s[0:1], -1, 0
	s_and_b64 s[2:3], s[6:7], s[0:1]
	s_andn2_b64 vcc, exec, s[2:3]
	s_cbranch_vccnz .LBB0_342
	s_waitcnt vmcnt(0)
	v_readlane_b32 s2, v254, 21
	s_barrier
	s_waitcnt vmcnt(9)
	v_mbcnt_lo_u32_b32 v0, -1, 0
	v_mbcnt_hi_u32_b32 v0, -1, v0
	s_nop 0
	v_cmp_eq_u32_e32 vcc, s2, v0
	s_and_saveexec_b64 s[2:3], vcc
	s_cbranch_execz .LBB0_341
	s_add_i32 s4, 0, 0x23d60
	v_mov_b32_e32 v0, s4
	s_waitcnt vmcnt(0) expcnt(0) lgkmcnt(0)
	ds_read_b32 v2, v0
	s_add_i32 s4, 0, 0x23d64
	v_mov_b32_e32 v0, s4
	ds_read_b32 v0, v0
	s_waitcnt lgkmcnt(1)
	v_cmp_ne_u32_e32 vcc, 0, v2
	s_cbranch_vccnz .LBB0_305
	v_readlane_b32 s4, v254, 0
	v_readlane_b32 s5, v254, 1
	s_load_dwordx2 s[8:9], s[4:5], 0x120
	s_load_dword s7, s[4:5], 0x128
	s_add_u32 s4, s92, 0x4200
	s_addc_u32 s5, s93, 0
	s_add_u32 s6, s92, 0x4400
	s_waitcnt lgkmcnt(0)
	s_mul_i32 s48, s9, s8
	s_mul_i32 s48, s48, s7
	s_addc_u32 s7, s93, 0
	s_add_u32 s8, s92, 0x4500
	s_addc_u32 s9, s93, 0
	s_add_u32 s10, s92, 0x4600
	s_addc_u32 s11, s93, 0
	s_add_u32 s12, s92, 0x4700
	s_addc_u32 s13, s93, 0
	s_add_u32 s14, s92, 0x4800
	s_addc_u32 s15, s93, 0
	s_add_u32 s16, s92, 0x4900
	s_addc_u32 s17, s93, 0
	s_add_u32 s18, s92, 0x4a00
	s_addc_u32 s19, s93, 0
	s_add_u32 s20, s92, 0x4b00
	s_addc_u32 s21, s93, 0
	s_add_u32 s22, s92, 0x4c00
	s_addc_u32 s23, s93, 0
	s_add_u32 s26, s92, 0x4d00
	s_addc_u32 s27, s93, 0
	s_add_u32 s28, s92, 0x4e00
	s_addc_u32 s29, s93, 0
	s_add_u32 s30, s92, 0x4f00
	s_addc_u32 s31, s93, 0
	s_add_u32 s34, s92, 0x5000
	s_addc_u32 s35, s93, 0
	s_add_u32 s36, s92, 0x5100
	s_addc_u32 s37, s93, 0
	s_add_u32 s38, s92, 0x5200
	s_addc_u32 s39, s93, 0
	s_add_u32 s40, s92, 0x5300
	s_addc_u32 s41, s93, 0
	s_mov_b32 s49, 1
	v_mov_b32_e32 v16, 0
	s_branch .LBB0_293

;     __host__ __device__ bool next(int i, Unit& u) const {
;         if (i > 0 && c < skew) return false;
;         const long L = (i == 0) ? (long)c : (long)G + (long)(i - 1) * (G - skew) + (c - skew); if (L >= nwg) return false;
;         int wgid = (int)L; { const int q = nwg / NXCD, r = nwg % NXCD, xcd = wgid % NXCD, off = wgid / NXCD; wgid = (xcd < r ? xcd * (q + 1) : r * (q + 1) + (xcd - r) * q) + off; }
;         const int nig = WGM * nN, gid = wgid / nig, fm = gid * WGM, gsz = (nM - fm) < WGM ? (nM - fm) : WGM;
;         u.pm = fm + ((wgid % nig) % gsz); u.pn = (wgid % nig) / gsz; u.pb = u.pn; u.po = u.pm; return true;
; template <class Epi, class Sched, bool ALIGN_EPI = false, bool SP2 = false, bool F8 = false, bool I8 = false, bool PF = false>
; __device__ __forceinline__ void gemm_phase(PG8_LAS unsigned char* lds, const Gemm g, const Sched& S, const Epi& E, const int wave_) {
;     ...
;     const int tid = tid_, wid = __builtin_amdgcn_readfirstlane(tid >> 6), lane = tid & 63, wr = wid >> 2, wc = wid & 3, fr = lane & 15, fq = lane >> 4;
;     const int K = g.K, nt = K / BK;
;     unsigned voffA[2], voffB[2];
; #pragma unroll
;     for (int i = 0; i < 2; ++i) { int R, C; stage_rc(tid * 16 + i * 8192, R, C); const int Rb = Epi::PERM ? ((R & ~31) + perm32(R & 31)) : R;
;         voffA[i] = (unsigned)(R * K + C) * 2u; voffB[i] = (unsigned)(Rb * K + C) * 2u; }
;     const size_t kstep = (size_t)(BK * 2);
;     const size_t hstep = (size_t)HALF * K * 2;
;     const size_t tstep = 2 * hstep;
;     const unsigned lds_a32 = (unsigned)(uintptr_t)lds;
;     const unsigned ldsw = (unsigned)wid * 1024u;
;     const int aoff = lds_byte(wr * 64 + fr, fq * 8), boff = lds_byte(wc * 32 + fr, fq * 8);
.LBB0_438:
	s_cmp_lt_i32 s94, 5
	s_cselect_b64 s[2:3], -1, 0
	s_add_u32 s60, s92, 0x5800000
	s_addc_u32 s61, s93, 0
	s_and_b64 s[0:1], s[2:3], s[0:1]
	s_andn2_b64 vcc, exec, s[0:1]
	s_cbranch_vccnz .LBB0_460
	s_cmp_lt_u32 s96, 0x100
	s_cbranch_scc1 .Lsp_4
	s_setprio 1
.Lsp_4:
	s_waitcnt vmcnt(9)
	v_mbcnt_lo_u32_b32 v0, -1, 0
	v_mbcnt_hi_u32_b32 v0, -1, v0
	s_cmpk_gt_i32 s33, 0x1ff
	v_add_u32_e32 v0, s96, v0
	s_nop 0
	v_mbcnt_lo_u32_b32 v0, -1, 0
	v_mbcnt_hi_u32_b32 v0, -1, v0
	s_waitcnt vmcnt(7)
	v_add_u32_e32 v9, s96, v0
	s_nop 0
	v_readfirstlane_b32 s3, v9
	s_cbranch_scc1 .LBB0_460
	v_lshlrev_b32_e32 v0, 4, v9
	v_add_u32_e32 v1, 0x2000, v0
	v_ashrrev_i32_e32 v2, 31, v1
	v_lshrrev_b32_e32 v2, 22, v2
	v_add_u32_e32 v2, v1, v2
	v_ashrrev_i32_e32 v8, 10, v2
	v_mul_i32_i24_e32 v2, 0x400, v8
	v_sub_u32_e32 v1, v1, v2
	v_lshrrev_b32_e32 v2, 4, v1
	v_bitop3_b32 v1, v2, v1, 32 bitop3:0x6c
	v_ashrrev_i32_e32 v2, 31, v1
	v_lshrrev_b32_e32 v2, 26, v2
	v_add_u32_e32 v2, v1, v2
	v_lshlrev_b32_e32 v3, 3, v8
	v_ashrrev_i32_e32 v10, 6, v2
	v_and_b32_e32 v3, -16, v3
	v_add_u32_e32 v3, v10, v3
	v_and_b32_e32 v4, 3, v10
	s_mov_b32 s2, 0x1fffe0
	v_lshrrev_b32_e32 v5, 2, v3
	v_lshlrev_b32_e32 v6, 1, v3
	v_and_b32_e32 v2, 0xc0, v2
	v_and_or_b32 v4, v3, s2, v4
	v_and_b32_e32 v5, 4, v5
	v_and_b32_e32 v6, 24, v6
	v_sub_u32_e32 v1, v1, v2
	v_mov_b32_e32 v2, 1
	v_or3_b32 v4, v4, v5, v6
	v_lshlrev_b32_e32 v5, 5, v8
	v_ashrrev_i16_sdwa v1, v2, sext(v1) dst_sel:DWORD dst_unused:UNUSED_PAD src0_sel:DWORD src1_sel:BYTE_0
	v_and_b32_e32 v5, 32, v5
	v_bfe_i32 v11, v1, 0, 16
	v_add_lshl_u32 v1, v5, v11, 1
	v_lshl_add_u32 v152, v4, 11, v1
	v_lshl_add_u32 v154, v3, 11, v1
	v_bfe_i32 v1, v9, 27, 1
	v_lshrrev_b32_e32 v1, 22, v1
	v_add_u32_e32 v1, v0, v1
	v_and_b32_e32 v1, 0xfffffc00, v1
	v_sub_u32_e32 v0, v0, v1
	v_lshrrev_b32_e32 v1, 4, v0
	v_ashrrev_i32_e32 v3, 31, v9
	v_bitop3_b32 v0, v1, v0, 32 bitop3:0x6c
	v_lshrrev_b32_e32 v3, 26, v3
	v_ashrrev_i32_e32 v1, 31, v0
	v_add_u32_e32 v3, v9, v3
	v_lshrrev_b32_e32 v1, 26, v1
	s_waitcnt vmcnt(6)
	v_ashrrev_i32_e32 v13, 6, v3
	v_add_u32_e32 v1, v0, v1
	v_lshlrev_b32_e32 v3, 3, v13
	v_ashrrev_i32_e32 v12, 6, v1
	v_and_b32_e32 v3, -16, v3
	s_add_u32 s34, s92, 0x1ed80000
	v_add_u32_e32 v3, v12, v3
	v_and_b32_e32 v4, 3, v12
	s_addc_u32 s35, s93, 0
	v_and_or_b32 v4, v3, s2, v4
	s_ashr_i32 s2, s33, 31
	s_lshr_b32 s2, s2, 29
	s_add_i32 s2, s33, s2
	s_ashr_i32 s4, s2, 3
	s_and_b32 s2, s2, -8
	s_ashr_i32 s6, s3, 6
	s_sub_i32 s2, s33, s2
	s_ashr_i32 s7, s3, 8
	s_lshl_b32 s36, s6, 10
	s_lshl_b32 s8, s2, 6
	s_mul_i32 s5, s2, 0x41
	s_cmp_lt_i32 s2, 0
	s_cselect_b32 s2, s5, s8
	s_add_i32 s2, s2, s4
	s_ashr_i32 s4, s2, 31
	s_lshr_b32 s4, s4, 27
	s_add_i32 s4, s2, s4
	s_ashr_i32 s5, s4, 5
	s_and_b32 s4, s4, 0xffe0
	s_sub_i32 s4, s2, s4
	s_bfe_i32 s2, s4, 0x80000
	s_bfe_u32 s2, s2, 0x3000c
	s_add_i32 s8, s4, s2
	s_bfe_i32 s2, s8, 0x80000
	s_and_b32 s8, s8, 0xf8
	s_sub_i32 s4, s4, s8
	s_lshl_b32 s5, s5, 3
	s_sext_i32_i16 s2, s2
	s_sext_i32_i8 s4, s4
	v_lshrrev_b32_e32 v5, 2, v3
	v_lshlrev_b32_e32 v6, 1, v3
	v_and_b32_e32 v1, 0xc0, v1
	s_lshr_b32 s2, s2, 3
	s_add_i32 s20, s5, s4
	v_and_b32_e32 v5, 4, v5
	v_and_b32_e32 v6, 24, v6
	v_sub_u32_e32 v0, v0, v1
	s_ashr_i32 s21, s20, 31
	s_bfe_i64 s[8:9], s[2:3], 0x100000
	v_or3_b32 v4, v4, v5, v6
	v_lshlrev_b32_e32 v5, 5, v13
	v_ashrrev_i16_sdwa v0, v2, sext(v0) dst_sel:DWORD dst_unused:UNUSED_PAD src0_sel:DWORD src1_sel:BYTE_0
	s_lshl_b64 s[4:5], s[20:21], 19
	s_lshl_b64 s[8:9], s[8:9], 19
	v_and_b32_e32 v5, 32, v5
	v_bfe_i32 v14, v0, 0, 16
	s_add_u32 s28, s34, s8
	v_add_lshl_u32 v0, v5, v14, 1
	s_addc_u32 s29, s35, s9
	s_add_i32 s21, s36, 0
	v_lshl_add_u32 v156, v4, 11, v0
	s_add_i32 m0, s21, 0x10000
	v_lshl_add_u32 v158, v3, 11, v0
	global_load_lds_dwordx4 v156, s[28:29]
	s_add_i32 m0, s21, 0x12000
	s_add_u32 s8, s28, 0x40000
	global_load_lds_dwordx4 v152, s[28:29]
	s_addc_u32 s9, s29, 0
	s_add_i32 m0, s21, 0x14000
	v_mov_b32_e32 v157, 0
	global_load_lds_dwordx4 v156, s[8:9]
	s_add_i32 m0, s21, 0x16000
	s_add_u32 s22, s26, s4
	s_addc_u32 s23, s27, s5
	s_add_i32 s37, s21, 0x2000
	global_load_lds_dwordx4 v152, s[8:9]
	s_mov_b32 m0, s21
	s_add_u32 s4, s22, 0x40000
	global_load_lds_dwordx4 v158, s[22:23]
	s_mov_b32 m0, s37
	s_addc_u32 s5, s23, 0
	s_add_i32 s38, s21, 0x4000
	global_load_lds_dwordx4 v154, s[22:23]
	s_mov_b32 m0, s38
	s_add_i32 s39, s21, 0x6000
	global_load_lds_dwordx4 v158, s[4:5]
	s_mov_b32 m0, s39
	v_mov_b32_e32 v153, v157
	global_load_lds_dwordx4 v154, s[4:5]
	v_readlane_b32 s4, v254, 0
	v_readlane_b32 s5, v254, 1
	s_load_dword s41, s[4:5], 0x120
	v_mov_b32_e32 v159, v157
	v_mov_b32_e32 v155, v157
	s_cmp_eq_u32 s7, 1
	s_mov_b32 s40, 0
	v_lshl_add_u64 v[6:7], s[28:29], 0, v[156:157]
	v_lshl_add_u64 v[4:5], s[28:29], 0, v[152:153]
	v_lshl_add_u64 v[0:1], s[22:23], 0, v[158:159]
	s_cselect_b64 s[4:5], -1, 0
	s_cmp_lg_u32 s7, 1
	v_lshl_add_u64 v[2:3], s[22:23], 0, v[154:155]
	s_cbranch_scc1 .LBB0_442
	s_barrier

; __device__ __forceinline__ int tid_from_wave(int wave) { unsigned l_; asm volatile("v_mbcnt_lo_u32_b32 %0, -1, 0\n\tv_mbcnt_hi_u32_b32 %0, -1, %0" : "=v"(l_)); return wave * 64 + (int)l_; }
; __device__ __forceinline__ unsigned xb_ld(unsigned* p)              { return __hip_atomic_load(p, __ATOMIC_RELAXED, __HIP_MEMORY_SCOPE_AGENT); }
; __device__ __forceinline__ unsigned xb_add(unsigned* p, unsigned v) { return __hip_atomic_fetch_add(p, v, __ATOMIC_RELAXED, __HIP_MEMORY_SCOPE_AGENT); }
; __device__ __forceinline__ void xcd_barrier_complete(unsigned* bar, unsigned x, unsigned& nloc, unsigned& nx) {
;     const unsigned G = gridDim.x * gridDim.y * gridDim.z;
;     unsigned sum, cnt, mine, sp = 0u;
;     for (;;) {
;         sum = 0u; cnt = 0u; mine = 0u;
; #pragma unroll
;         for (unsigned j = 0; j < 16; ++j) { const unsigned c = xb_ld(&bar[XB_XCNT(j)]); sum += c; cnt += (c > 0u) ? 1u : 0u; mine = (j == x) ? c : mine; }
;         if (sum == G) break;
;         __builtin_amdgcn_s_sleep(1);
;         if ((++sp & 255u) == 0u) { if (xb_ld(&bar[XB_TMO])) break; if (sp > XB_SPIN_CAP) { atomicAdd(&bar[XB_TMO], 1u); break; } }
; __device__ __forceinline__ void xcd_barrier(const XcdBarrier& b) {
;     asm volatile("s_waitcnt vmcnt(0)" ::: "memory");
;     __syncthreads();
;     if (tid_from_wave(b.wave) == 0) {
;         unsigned* bar = b.bar;
;         __builtin_amdgcn_s_waitcnt(0);
;         unsigned nloc = b.st[0], nx = b.st[1];
;         if (nloc == 0u) { xcd_barrier_complete(bar, b.x, nloc, nx); b.st[0] = nloc; b.st[1] = nx; }
;         const unsigned old = xb_add(&bar[XB_XSUB(b.x)], 1u);
.LBB0_460:
	s_setprio 0
	s_cmp_gt_i32 s95, 5
	s_cselect_b64 s[2:3], -1, 0
	s_and_b64 s[0:1], s[0:1], s[2:3]
	s_andn2_b64 vcc, exec, s[0:1]
	s_cbranch_vccnz .LBB0_514
	s_waitcnt vmcnt(0)
	v_readlane_b32 s0, v254, 21
	s_barrier
	s_waitcnt vmcnt(9)
	v_mbcnt_lo_u32_b32 v0, -1, 0
	v_mbcnt_hi_u32_b32 v0, -1, v0
	s_nop 0
	v_cmp_eq_u32_e32 vcc, s0, v0
	s_and_saveexec_b64 s[0:1], vcc
	s_cbranch_execz .LBB0_513
	s_add_i32 s4, 0, 0x23d60
	v_mov_b32_e32 v0, s4
	s_waitcnt vmcnt(0) expcnt(0) lgkmcnt(0)
	ds_read_b32 v2, v0
	s_add_i32 s4, 0, 0x23d64
	v_mov_b32_e32 v0, s4
	ds_read_b32 v0, v0
	s_waitcnt lgkmcnt(1)
	v_cmp_ne_u32_e32 vcc, 0, v2
	s_cbranch_vccnz .LBB0_477
	v_readlane_b32 s4, v254, 0
	v_readlane_b32 s5, v254, 1
	s_load_dwordx2 s[8:9], s[4:5], 0x120
	s_load_dword s7, s[4:5], 0x128
	s_add_u32 s4, s92, 0x4200
	s_addc_u32 s5, s93, 0
	s_add_u32 s6, s92, 0x4400
	s_waitcnt lgkmcnt(0)
	s_mul_i32 s48, s9, s8
	s_mul_i32 s48, s48, s7
	s_addc_u32 s7, s93, 0
	s_add_u32 s8, s92, 0x4500
	s_addc_u32 s9, s93, 0
	s_add_u32 s10, s92, 0x4600
	s_addc_u32 s11, s93, 0
	s_add_u32 s12, s92, 0x4700
	s_addc_u32 s13, s93, 0
	s_add_u32 s14, s92, 0x4800
	s_addc_u32 s15, s93, 0
	s_add_u32 s16, s92, 0x4900
	s_addc_u32 s17, s93, 0
	s_add_u32 s18, s92, 0x4a00
	s_addc_u32 s19, s93, 0
	s_add_u32 s20, s92, 0x4b00
	s_addc_u32 s21, s93, 0
	s_add_u32 s22, s92, 0x4c00
	s_addc_u32 s23, s93, 0
	s_add_u32 s26, s92, 0x4d00
	s_addc_u32 s27, s93, 0
	s_add_u32 s28, s92, 0x4e00
	s_addc_u32 s29, s93, 0
	s_add_u32 s30, s92, 0x4f00
	s_addc_u32 s31, s93, 0
	s_add_u32 s34, s92, 0x5000
	s_addc_u32 s35, s93, 0
	s_add_u32 s36, s92, 0x5100
	s_addc_u32 s37, s93, 0
	s_add_u32 s38, s92, 0x5200
	s_addc_u32 s39, s93, 0
	s_add_u32 s40, s92, 0x5300
	s_addc_u32 s41, s93, 0
	s_mov_b32 s49, 1
	v_mov_b32_e32 v16, 0
	s_branch .LBB0_465

;     __host__ __device__ bool next(int i, Unit& u) const {
;         if (i > 0 && c < skew) return false;
;         const long L = (i == 0) ? (long)c : (long)G + (long)(i - 1) * (G - skew) + (c - skew); if (L >= nwg) return false;
;         int wgid = (int)L; { const int q = nwg / NXCD, r = nwg % NXCD, xcd = wgid % NXCD, off = wgid / NXCD; wgid = (xcd < r ? xcd * (q + 1) : r * (q + 1) + (xcd - r) * q) + off; }
;         const int nig = WGM * nN, gid = wgid / nig, fm = gid * WGM, gsz = (nM - fm) < WGM ? (nM - fm) : WGM;
;         u.pm = fm + ((wgid % nig) % gsz); u.pn = (wgid % nig) / gsz; u.pb = u.pn; u.po = u.pm; return true;
; template <class Epi, class Sched, bool ALIGN_EPI = false, bool SP2 = false, bool F8 = false, bool I8 = false, bool PF = false>
; __device__ __forceinline__ void gemm_phase(PG8_LAS unsigned char* lds, const Gemm g, const Sched& S, const Epi& E, const int wave_) {
;     ...
;     const int tid = tid_, wid = __builtin_amdgcn_readfirstlane(tid >> 6), lane = tid & 63, wr = wid >> 2, wc = wid & 3, fr = lane & 15, fq = lane >> 4;
;     const int K = g.K, nt = K / BK;
;     unsigned voffA[2], voffB[2];
; #pragma unroll
;     for (int i = 0; i < 2; ++i) { int R, C; stage_rc(tid * 16 + i * 8192, R, C); const int Rb = Epi::PERM ? ((R & ~31) + perm32(R & 31)) : R;
;         voffA[i] = (unsigned)(R * K + C) * 2u; voffB[i] = (unsigned)(Rb * K + C) * 2u; }
;     const size_t kstep = (size_t)(BK * 2);
;     const size_t hstep = (size_t)HALF * K * 2;
;     const size_t tstep = 2 * hstep;
;     const unsigned lds_a32 = (unsigned)(uintptr_t)lds;
;     const unsigned ldsw = (unsigned)wid * 1024u;
;     const int aoff = lds_byte(wr * 64 + fr, fq * 8), boff = lds_byte(wc * 32 + fr, fq * 8);
.LBB0_580:
	s_cmp_lt_i32 s94, 7
	s_cselect_b64 s[0:1], -1, 0
	s_and_b64 s[0:1], s[0:1], s[2:3]
	s_andn2_b64 vcc, exec, s[0:1]
	s_cbranch_vccnz .LBB0_598
	s_cmp_lt_u32 s96, 0x100
	s_cbranch_scc1 .Lsp_6
	s_setprio 1
.Lsp_6:
	s_waitcnt vmcnt(9)
	v_mbcnt_lo_u32_b32 v0, -1, 0
	v_mbcnt_hi_u32_b32 v0, -1, v0
	s_cmpk_gt_i32 s33, 0xaff
	v_add_u32_e32 v0, s96, v0
	s_nop 0
	v_mbcnt_lo_u32_b32 v0, -1, 0
	v_mbcnt_hi_u32_b32 v0, -1, v0
	s_waitcnt vmcnt(7)
	v_add_u32_e32 v9, s96, v0
	s_nop 0
	v_readfirstlane_b32 s3, v9
	s_cbranch_scc1 .LBB0_598
	v_lshlrev_b32_e32 v0, 4, v9
	v_add_u32_e32 v1, 0x2000, v0
	v_ashrrev_i32_e32 v2, 31, v1
	v_lshrrev_b32_e32 v2, 22, v2
	v_add_u32_e32 v2, v1, v2
	v_ashrrev_i32_e32 v8, 10, v2
	v_mul_i32_i24_e32 v2, 0x400, v8
	v_sub_u32_e32 v1, v1, v2
	v_lshrrev_b32_e32 v2, 4, v1
	v_bitop3_b32 v1, v2, v1, 32 bitop3:0x6c
	v_ashrrev_i32_e32 v2, 31, v1
	v_lshrrev_b32_e32 v2, 26, v2
	v_add_u32_e32 v2, v1, v2
	v_lshlrev_b32_e32 v3, 3, v8
	v_ashrrev_i32_e32 v10, 6, v2
	v_and_b32_e32 v3, -16, v3
	v_add_u32_e32 v3, v10, v3
	v_and_b32_e32 v4, 3, v10
	s_mov_b32 s2, 0x3fffe0
	v_lshrrev_b32_e32 v5, 2, v3
	v_lshlrev_b32_e32 v6, 1, v3
	v_and_b32_e32 v2, 0xc0, v2
	v_and_or_b32 v4, v3, s2, v4
	v_and_b32_e32 v5, 4, v5
	v_and_b32_e32 v6, 24, v6
	v_sub_u32_e32 v1, v1, v2
	v_mov_b32_e32 v2, 1
	v_or3_b32 v4, v4, v5, v6
	v_lshlrev_b32_e32 v5, 5, v8
	v_ashrrev_i16_sdwa v1, v2, sext(v1) dst_sel:DWORD dst_unused:UNUSED_PAD src0_sel:DWORD src1_sel:BYTE_0
	v_and_b32_e32 v5, 32, v5
	v_bfe_i32 v11, v1, 0, 16
	v_add_lshl_u32 v1, v5, v11, 1
	v_lshl_add_u32 v128, v4, 10, v1
	v_lshl_add_u32 v130, v3, 10, v1
	v_bfe_i32 v1, v9, 27, 1
	v_lshrrev_b32_e32 v1, 22, v1
	v_add_u32_e32 v1, v0, v1
	v_and_b32_e32 v1, 0xfffffc00, v1
	v_sub_u32_e32 v0, v0, v1
	v_lshrrev_b32_e32 v1, 4, v0
	v_ashrrev_i32_e32 v3, 31, v9
	v_bitop3_b32 v0, v1, v0, 32 bitop3:0x6c
	v_lshrrev_b32_e32 v3, 26, v3
	v_ashrrev_i32_e32 v1, 31, v0
	v_add_u32_e32 v3, v9, v3
	v_lshrrev_b32_e32 v1, 26, v1
	s_waitcnt vmcnt(6)
	v_ashrrev_i32_e32 v13, 6, v3
	v_add_u32_e32 v1, v0, v1
	v_lshlrev_b32_e32 v3, 3, v13
	v_ashrrev_i32_e32 v12, 6, v1
	v_and_b32_e32 v3, -16, v3
	s_add_u32 s15, s92, 0x1ef80000
	v_add_u32_e32 v3, v12, v3
	v_and_b32_e32 v4, 3, v12
	s_addc_u32 s38, s93, 0
	v_and_or_b32 v4, v3, s2, v4
	s_ashr_i32 s2, s33, 31
	s_lshr_b32 s2, s2, 29
	s_add_i32 s2, s33, s2
	s_ashr_i32 s10, s3, 6
	s_ashr_i32 s4, s2, 3
	s_and_b32 s2, s2, -8
	s_ashr_i32 s11, s3, 8
	s_lshl_b32 s39, s10, 10
	s_sub_i32 s2, s33, s2
	s_cmp_lt_i32 s2, 0
	s_movk_i32 s40, 0x161
	s_cselect_b32 s5, s40, 0x160
	s_mul_i32 s2, s2, s5
	s_add_i32 s2, s2, s4
	s_mul_hi_i32 s4, s2, 0x2e8ba2e9
	s_lshr_b32 s5, s4, 31
	s_ashr_i32 s4, s4, 5
	s_add_i32 s4, s4, s5
	s_lshl_b32 s5, s4, 3
	s_mulk_i32 s4, 0xb0
	s_sub_i32 s4, s2, s4
	s_bfe_u32 s2, s4, 0x3001c
	s_add_i32 s6, s4, s2
	s_sext_i32_i16 s2, s6
	s_and_b32 s6, s6, 0xfff8
	s_sub_i32 s4, s4, s6
	s_sext_i32_i16 s4, s4
	v_lshrrev_b32_e32 v5, 2, v3
	v_lshlrev_b32_e32 v6, 1, v3
	v_and_b32_e32 v1, 0xc0, v1
	s_lshr_b32 s2, s2, 3
	s_add_i32 s28, s5, s4
	v_and_b32_e32 v5, 4, v5
	v_and_b32_e32 v6, 24, v6
	v_sub_u32_e32 v0, v0, v1
	s_ashr_i32 s29, s28, 31
	s_bfe_i64 s[6:7], s[2:3], 0x100000
	v_or3_b32 v4, v4, v5, v6
	v_lshlrev_b32_e32 v5, 5, v13
	v_ashrrev_i16_sdwa v0, v2, sext(v0) dst_sel:DWORD dst_unused:UNUSED_PAD src0_sel:DWORD src1_sel:BYTE_0
	s_lshl_b64 s[4:5], s[28:29], 18
	s_lshl_b64 s[6:7], s[6:7], 18
	v_and_b32_e32 v5, 32, v5
	v_bfe_i32 v14, v0, 0, 16
	s_add_u32 s34, s15, s6
	v_add_lshl_u32 v0, v5, v14, 1
	s_addc_u32 s35, s38, s7
	s_add_i32 s29, s39, 0
	v_lshl_add_u32 v132, v4, 10, v0
	s_add_i32 m0, s29, 0x10000
	v_lshl_add_u32 v134, v3, 10, v0
	global_load_lds_dwordx4 v132, s[34:35]
	s_add_i32 m0, s29, 0x12000
	s_add_u32 s6, s34, 0x20000
	global_load_lds_dwordx4 v128, s[34:35]
	s_addc_u32 s7, s35, 0
	s_add_i32 m0, s29, 0x14000
	v_mov_b32_e32 v133, 0
	global_load_lds_dwordx4 v132, s[6:7]
	s_add_i32 m0, s29, 0x16000
	s_add_u32 s30, s58, s4
	s_addc_u32 s31, s59, s5
	s_add_i32 s41, s29, 0x2000
	global_load_lds_dwordx4 v128, s[6:7]
	s_mov_b32 m0, s29
	s_add_u32 s4, s30, 0x20000
	global_load_lds_dwordx4 v134, s[30:31]
	s_mov_b32 m0, s41
	s_addc_u32 s5, s31, 0
	s_add_i32 s42, s29, 0x4000
	global_load_lds_dwordx4 v130, s[30:31]
	s_mov_b32 m0, s42
	s_add_i32 s43, s29, 0x6000
	global_load_lds_dwordx4 v134, s[4:5]
	s_mov_b32 m0, s43
	v_mov_b32_e32 v129, v133
	global_load_lds_dwordx4 v130, s[4:5]
	v_readlane_b32 s4, v254, 0
	v_readlane_b32 s5, v254, 1
	s_load_dword s45, s[4:5], 0x120
	v_mov_b32_e32 v135, v133
	v_mov_b32_e32 v131, v133
	s_cmp_eq_u32 s11, 1
	s_mov_b32 s44, 0
	v_lshl_add_u64 v[6:7], s[34:35], 0, v[132:133]
	v_lshl_add_u64 v[4:5], s[34:35], 0, v[128:129]
	v_lshl_add_u64 v[0:1], s[30:31], 0, v[134:135]
	s_cselect_b64 s[4:5], -1, 0
	s_cmp_lg_u32 s11, 1
	v_lshl_add_u64 v[2:3], s[30:31], 0, v[130:131]
	s_cbranch_scc1 .LBB0_584
	s_barrier

; __device__ __forceinline__ int tid_from_wave(int wave) { unsigned l_; asm volatile("v_mbcnt_lo_u32_b32 %0, -1, 0\n\tv_mbcnt_hi_u32_b32 %0, -1, %0" : "=v"(l_)); return wave * 64 + (int)l_; }
; __device__ __forceinline__ unsigned xb_ld(unsigned* p)              { return __hip_atomic_load(p, __ATOMIC_RELAXED, __HIP_MEMORY_SCOPE_AGENT); }
; __device__ __forceinline__ unsigned xb_add(unsigned* p, unsigned v) { return __hip_atomic_fetch_add(p, v, __ATOMIC_RELAXED, __HIP_MEMORY_SCOPE_AGENT); }
; __device__ __forceinline__ void xcd_barrier_complete(unsigned* bar, unsigned x, unsigned& nloc, unsigned& nx) {
;     const unsigned G = gridDim.x * gridDim.y * gridDim.z;
;     unsigned sum, cnt, mine, sp = 0u;
;     for (;;) {
;         sum = 0u; cnt = 0u; mine = 0u;
; #pragma unroll
;         for (unsigned j = 0; j < 16; ++j) { const unsigned c = xb_ld(&bar[XB_XCNT(j)]); sum += c; cnt += (c > 0u) ? 1u : 0u; mine = (j == x) ? c : mine; }
;         if (sum == G) break;
;         __builtin_amdgcn_s_sleep(1);
;         if ((++sp & 255u) == 0u) { if (xb_ld(&bar[XB_TMO])) break; if (sp > XB_SPIN_CAP) { atomicAdd(&bar[XB_TMO], 1u); break; } }
; __device__ __forceinline__ void xcd_barrier(const XcdBarrier& b) {
;     asm volatile("s_waitcnt vmcnt(0)" ::: "memory");
;     __syncthreads();
;     if (tid_from_wave(b.wave) == 0) {
;         unsigned* bar = b.bar;
;         __builtin_amdgcn_s_waitcnt(0);
;         unsigned nloc = b.st[0], nx = b.st[1];
;         if (nloc == 0u) { xcd_barrier_complete(bar, b.x, nloc, nx); b.st[0] = nloc; b.st[1] = nx; }
;         const unsigned old = xb_add(&bar[XB_XSUB(b.x)], 1u);
.LBB0_598:
	s_setprio 0
	s_cmp_gt_i32 s95, 7
	s_cselect_b64 s[2:3], -1, 0
	s_and_b64 s[0:1], s[0:1], s[2:3]
	s_andn2_b64 vcc, exec, s[0:1]
	s_cbranch_vccnz .LBB0_652
	s_waitcnt vmcnt(0)
	v_readlane_b32 s0, v254, 21
	s_barrier
	s_waitcnt vmcnt(9)
	v_mbcnt_lo_u32_b32 v0, -1, 0
	v_mbcnt_hi_u32_b32 v0, -1, v0
	s_nop 0
	v_cmp_eq_u32_e32 vcc, s0, v0
	s_and_saveexec_b64 s[0:1], vcc
	s_cbranch_execz .LBB0_651
	s_add_i32 s4, 0, 0x23d60
	v_mov_b32_e32 v0, s4
	s_waitcnt vmcnt(0) expcnt(0) lgkmcnt(0)
	ds_read_b32 v2, v0
	s_add_i32 s4, 0, 0x23d64
	v_mov_b32_e32 v0, s4
	ds_read_b32 v0, v0
	s_waitcnt lgkmcnt(1)
	v_cmp_ne_u32_e32 vcc, 0, v2
	s_cbranch_vccnz .LBB0_615
	v_readlane_b32 s4, v254, 0
	v_readlane_b32 s5, v254, 1
	s_load_dwordx2 s[8:9], s[4:5], 0x120
	s_load_dword s7, s[4:5], 0x128
	s_add_u32 s4, s92, 0x4200
	s_addc_u32 s5, s93, 0
	s_add_u32 s6, s92, 0x4400
	s_waitcnt lgkmcnt(0)
	s_mul_i32 s48, s9, s8
	s_mul_i32 s48, s48, s7
	s_addc_u32 s7, s93, 0
	s_add_u32 s8, s92, 0x4500
	s_addc_u32 s9, s93, 0
	s_add_u32 s10, s92, 0x4600
	s_addc_u32 s11, s93, 0
	s_add_u32 s12, s92, 0x4700
	s_addc_u32 s13, s93, 0
	s_add_u32 s14, s92, 0x4800
	s_addc_u32 s15, s93, 0
	s_add_u32 s16, s92, 0x4900
	s_addc_u32 s17, s93, 0
	s_add_u32 s18, s92, 0x4a00
	s_addc_u32 s19, s93, 0
	s_add_u32 s20, s92, 0x4b00
	s_addc_u32 s21, s93, 0
	s_add_u32 s22, s92, 0x4c00
	s_addc_u32 s23, s93, 0
	s_add_u32 s26, s92, 0x4d00
	s_addc_u32 s27, s93, 0
	s_add_u32 s28, s92, 0x4e00
	s_addc_u32 s29, s93, 0
	s_add_u32 s30, s92, 0x4f00
	s_addc_u32 s31, s93, 0
	s_add_u32 s34, s92, 0x5000
	s_addc_u32 s35, s93, 0
	s_add_u32 s36, s92, 0x5100
	s_addc_u32 s37, s93, 0
	s_add_u32 s38, s92, 0x5200
	s_addc_u32 s39, s93, 0
	s_add_u32 s40, s92, 0x5300
	s_addc_u32 s41, s93, 0
	s_mov_b32 s49, 1
	v_mov_b32_e32 v16, 0
	s_branch .LBB0_603

;     __host__ __device__ bool next(int i, Unit& u) const {
;         if (i > 0 && c < skew) return false;
;         const long L = (i == 0) ? (long)c : (long)G + (long)(i - 1) * (G - skew) + (c - skew); if (L >= nwg) return false;
;         int wgid = (int)L; { const int q = nwg / NXCD, r = nwg % NXCD, xcd = wgid % NXCD, off = wgid / NXCD; wgid = (xcd < r ? xcd * (q + 1) : r * (q + 1) + (xcd - r) * q) + off; }
;         const int nig = WGM * nN, gid = wgid / nig, fm = gid * WGM, gsz = (nM - fm) < WGM ? (nM - fm) : WGM;
;         u.pm = fm + ((wgid % nig) % gsz); u.pn = (wgid % nig) / gsz; u.pb = u.pn; u.po = u.pm; return true;
; template <class Epi, class Sched, bool ALIGN_EPI = false, bool SP2 = false, bool F8 = false, bool I8 = false, bool PF = false>
; __device__ __forceinline__ void gemm_phase(PG8_LAS unsigned char* lds, const Gemm g, const Sched& S, const Epi& E, const int wave_) {
;     ...
;     const int tid = tid_, wid = __builtin_amdgcn_readfirstlane(tid >> 6), lane = tid & 63, wr = wid >> 2, wc = wid & 3, fr = lane & 15, fq = lane >> 4;
;     const int K = g.K, nt = K / BK;
;     unsigned voffA[2], voffB[2];
; #pragma unroll
;     for (int i = 0; i < 2; ++i) { int R, C; stage_rc(tid * 16 + i * 8192, R, C); const int Rb = Epi::PERM ? ((R & ~31) + perm32(R & 31)) : R;
;         voffA[i] = (unsigned)(R * K + C) * 2u; voffB[i] = (unsigned)(Rb * K + C) * 2u; }
;     const size_t kstep = (size_t)(BK * 2);
;     const size_t hstep = (size_t)HALF * K * 2;
;     const size_t tstep = 2 * hstep;
;     const unsigned lds_a32 = (unsigned)(uintptr_t)lds;
;     const unsigned ldsw = (unsigned)wid * 1024u;
;     const int aoff = lds_byte(wr * 64 + fr, fq * 8), boff = lds_byte(wc * 32 + fr, fq * 8);
.LBB0_652:
	s_cmp_lt_i32 s94, 8
	s_cselect_b64 s[0:1], -1, 0
	s_and_b64 s[0:1], s[0:1], s[2:3]
	s_andn2_b64 vcc, exec, s[0:1]
	s_cbranch_vccnz .LBB0_678
	s_cmp_lt_u32 s96, 0x100
	s_cbranch_scc1 .Lsp_7
	s_setprio 1
.Lsp_7:
	s_waitcnt vmcnt(9)
	v_mbcnt_lo_u32_b32 v0, -1, 0
	v_mbcnt_hi_u32_b32 v0, -1, v0
	s_cmpk_gt_i32 s33, 0x1ff
	v_add_u32_e32 v0, s96, v0
	s_nop 0
	v_mbcnt_lo_u32_b32 v0, -1, 0
	v_mbcnt_hi_u32_b32 v0, -1, v0
	s_waitcnt vmcnt(7)
	v_add_u32_e32 v9, s96, v0
	s_nop 0
	v_readfirstlane_b32 s2, v9
	s_cbranch_scc1 .LBB0_678
	v_lshlrev_b32_e32 v0, 4, v9
	v_add_u32_e32 v1, 0x2000, v0
	v_ashrrev_i32_e32 v2, 31, v1
	v_lshrrev_b32_e32 v2, 22, v2
	v_add_u32_e32 v2, v1, v2
	v_ashrrev_i32_e32 v8, 10, v2
	v_mul_i32_i24_e32 v2, 0x400, v8
	v_sub_u32_e32 v1, v1, v2
	v_lshrrev_b32_e32 v2, 4, v1
	v_bitop3_b32 v1, v2, v1, 32 bitop3:0x6c
	v_ashrrev_i32_e32 v2, 31, v1
	v_lshrrev_b32_e32 v2, 26, v2
	v_add_u32_e32 v2, v1, v2
	v_lshlrev_b32_e32 v3, 3, v8
	v_ashrrev_i32_e32 v10, 6, v2
	v_and_b32_e32 v3, -16, v3
	v_add_u32_e32 v3, v10, v3
	v_and_b32_e32 v4, 3, v10
	s_mov_b32 s6, 0x1ffffe0
	v_lshrrev_b32_e32 v5, 2, v3
	v_lshlrev_b32_e32 v6, 1, v3
	v_and_b32_e32 v2, 0xc0, v2
	v_and_or_b32 v4, v3, s6, v4
	v_and_b32_e32 v5, 4, v5
	v_and_b32_e32 v6, 24, v6
	v_sub_u32_e32 v1, v1, v2
	v_mov_b32_e32 v2, 1
	v_or3_b32 v4, v4, v5, v6
	v_lshlrev_b32_e32 v5, 5, v8
	v_ashrrev_i16_sdwa v1, v2, sext(v1) dst_sel:DWORD dst_unused:UNUSED_PAD src0_sel:DWORD src1_sel:BYTE_0
	s_movk_i32 s3, 0x580
	v_and_b32_e32 v11, 32, v5
	s_waitcnt vmcnt(6)
	v_bfe_i32 v12, v1, 0, 16
	v_mul_lo_u32 v4, v4, s3
	v_add_u32_e32 v1, v11, v12
	v_mul_lo_u32 v3, v3, s3
	v_add_lshl_u32 v164, v4, v1, 1
	v_add_lshl_u32 v166, v1, v3, 1
	v_bfe_i32 v1, v9, 27, 1
	v_lshrrev_b32_e32 v1, 22, v1
	v_add_u32_e32 v1, v0, v1
	v_and_b32_e32 v1, 0xfffffc00, v1
	v_sub_u32_e32 v0, v0, v1
	v_lshrrev_b32_e32 v1, 4, v0
	v_ashrrev_i32_e32 v3, 31, v9
	v_bitop3_b32 v0, v1, v0, 32 bitop3:0x6c
	v_lshrrev_b32_e32 v3, 26, v3
	v_ashrrev_i32_e32 v1, 31, v0
	v_add_u32_e32 v3, v9, v3
	v_lshrrev_b32_e32 v1, 26, v1
	v_ashrrev_i32_e32 v14, 6, v3
	v_add_u32_e32 v1, v0, v1
	v_lshlrev_b32_e32 v3, 3, v14
	v_ashrrev_i32_e32 v13, 6, v1
	v_and_b32_e32 v3, -16, v3
	s_add_u32 s15, s92, 0x1fa80000
	v_add_u32_e32 v3, v13, v3
	v_and_b32_e32 v4, 3, v13
	s_addc_u32 s38, s93, 0
	v_and_or_b32 v4, v3, s6, v4
	s_ashr_i32 s6, s33, 31
	s_lshr_b32 s6, s6, 29
	s_add_i32 s6, s33, s6
	s_ashr_i32 s7, s6, 3
	s_and_b32 s6, s6, -8
	s_ashr_i32 s4, s2, 6
	s_sub_i32 s6, s33, s6
	s_ashr_i32 s5, s2, 8
	s_lshl_b32 s39, s4, 10
	s_lshl_b32 s9, s6, 6
	s_mul_i32 s8, s6, 0x41
	s_cmp_lt_i32 s6, 0
	s_cselect_b32 s6, s8, s9
	s_add_i32 s6, s6, s7
	s_ashr_i32 s7, s6, 31
	s_lshr_b32 s7, s7, 27
	s_add_i32 s7, s6, s7
	s_ashr_i32 s8, s7, 5
	s_and_b32 s7, s7, 0xffe0
	s_sub_i32 s6, s6, s7
	s_bfe_i32 s7, s6, 0x80000
	s_bfe_u32 s7, s7, 0x3000c
	s_add_i32 s7, s6, s7
	s_bfe_i32 s9, s7, 0x80000
	s_and_b32 s7, s7, 0xf8
	s_sub_i32 s6, s6, s7
	v_lshrrev_b32_e32 v5, 2, v3
	v_lshlrev_b32_e32 v6, 1, v3
	v_and_b32_e32 v1, 0xc0, v1
	s_lshl_b32 s8, s8, 3
	s_sext_i32_i16 s9, s9
	s_sext_i32_i8 s6, s6
	v_and_b32_e32 v5, 4, v5
	v_and_b32_e32 v6, 24, v6
	v_sub_u32_e32 v0, v0, v1
	s_add_i32 s57, s8, s6
	s_ashr_i32 s6, s9, 3
	v_or3_b32 v4, v4, v5, v6
	v_lshlrev_b32_e32 v5, 5, v14
	v_ashrrev_i16_sdwa v0, v2, sext(v0) dst_sel:DWORD dst_unused:UNUSED_PAD src0_sel:DWORD src1_sel:BYTE_0
	s_lshr_b32 s12, s9, 3
	s_mul_hi_i32 s7, s6, 0xb0000
	s_mul_i32 s6, s6, 0xb0000
	v_and_b32_e32 v15, 32, v5
	s_waitcnt vmcnt(5)
	v_bfe_i32 v16, v0, 0, 16
	s_add_u32 s28, s15, s6
	v_mul_lo_u32 v4, v4, s3
	v_add_u32_e32 v0, v15, v16
	s_addc_u32 s29, s38, s7
	s_add_i32 s40, s39, 0
	v_add_lshl_u32 v168, v4, v0, 1
	s_add_i32 m0, s40, 0x10000
	s_mul_i32 s10, s57, 0xb0000
	global_load_lds_dwordx4 v168, s[28:29]
	s_add_i32 m0, s40, 0x12000
	s_add_u32 s6, s28, 0x58000
	global_load_lds_dwordx4 v164, s[28:29]
	s_addc_u32 s7, s29, 0
	s_add_i32 m0, s40, 0x14000
	s_mul_hi_i32 s8, s57, 0xb0000
	global_load_lds_dwordx4 v168, s[6:7]
	s_add_i32 m0, s40, 0x16000
	s_add_u32 s30, s24, s10
	v_mul_lo_u32 v1, v3, s3
	s_addc_u32 s31, s25, s8
	s_add_i32 s41, s40, 0x2000
	v_add_lshl_u32 v170, v0, v1, 1
	global_load_lds_dwordx4 v164, s[6:7]
	s_mov_b32 m0, s40
	s_add_u32 s6, s30, 0x58000
	global_load_lds_dwordx4 v170, s[30:31]
	s_mov_b32 m0, s41
	s_addc_u32 s7, s31, 0
	s_add_i32 s42, s40, 0x4000
	global_load_lds_dwordx4 v166, s[30:31]
	s_mov_b32 m0, s42
	s_add_i32 s43, s40, 0x6000
	global_load_lds_dwordx4 v170, s[6:7]
	s_mov_b32 m0, s43
	v_mov_b32_e32 v169, 0
	global_load_lds_dwordx4 v166, s[6:7]
	v_readlane_b32 s6, v254, 0
	v_readlane_b32 s7, v254, 1
	s_load_dword s45, s[6:7], 0x120
	v_mov_b32_e32 v165, v169
	v_mov_b32_e32 v171, v169
	v_mov_b32_e32 v167, v169
	s_cmp_eq_u32 s5, 1
	s_mov_b32 s44, 0
	v_lshl_add_u64 v[6:7], s[28:29], 0, v[168:169]
	v_lshl_add_u64 v[2:3], s[28:29], 0, v[164:165]
	s_mov_b64 s[6:7], 0x58000
	v_lshl_add_u64 v[0:1], s[30:31], 0, v[170:171]
	s_cselect_b64 s[8:9], -1, 0
	s_cmp_lg_u32 s5, 1
	v_lshl_add_u64 v[4:5], s[30:31], 0, v[166:167]
	s_cbranch_scc1 .LBB0_656
	s_barrier

; __device__ __forceinline__ int tid_from_wave(int wave) { unsigned l_; asm volatile("v_mbcnt_lo_u32_b32 %0, -1, 0\n\tv_mbcnt_hi_u32_b32 %0, -1, %0" : "=v"(l_)); return wave * 64 + (int)l_; }
; __device__ __forceinline__ unsigned xb_ld(unsigned* p)              { return __hip_atomic_load(p, __ATOMIC_RELAXED, __HIP_MEMORY_SCOPE_AGENT); }
; __device__ __forceinline__ unsigned xb_add(unsigned* p, unsigned v) { return __hip_atomic_fetch_add(p, v, __ATOMIC_RELAXED, __HIP_MEMORY_SCOPE_AGENT); }
; __device__ __forceinline__ void xcd_barrier_complete(unsigned* bar, unsigned x, unsigned& nloc, unsigned& nx) {
;     const unsigned G = gridDim.x * gridDim.y * gridDim.z;
;     unsigned sum, cnt, mine, sp = 0u;
;     for (;;) {
;         sum = 0u; cnt = 0u; mine = 0u;
; #pragma unroll
;         for (unsigned j = 0; j < 16; ++j) { const unsigned c = xb_ld(&bar[XB_XCNT(j)]); sum += c; cnt += (c > 0u) ? 1u : 0u; mine = (j == x) ? c : mine; }
;         if (sum == G) break;
;         __builtin_amdgcn_s_sleep(1);
;         if ((++sp & 255u) == 0u) { if (xb_ld(&bar[XB_TMO])) break; if (sp > XB_SPIN_CAP) { atomicAdd(&bar[XB_TMO], 1u); break; } }
; __device__ __forceinline__ void xcd_barrier(const XcdBarrier& b) {
;     asm volatile("s_waitcnt vmcnt(0)" ::: "memory");
;     __syncthreads();
;     if (tid_from_wave(b.wave) == 0) {
;         unsigned* bar = b.bar;
;         __builtin_amdgcn_s_waitcnt(0);
;         unsigned nloc = b.st[0], nx = b.st[1];
;         if (nloc == 0u) { xcd_barrier_complete(bar, b.x, nloc, nx); b.st[0] = nloc; b.st[1] = nx; }
;         const unsigned old = xb_add(&bar[XB_XSUB(b.x)], 1u);
.LBB0_678:
	s_setprio 0
	s_cmp_gt_i32 s95, 8
	s_cselect_b64 s[2:3], -1, 0
	s_and_b64 s[0:1], s[0:1], s[2:3]
	s_andn2_b64 vcc, exec, s[0:1]
	s_cbranch_vccnz .LBB0_732
	s_waitcnt vmcnt(0)
	v_readlane_b32 s0, v254, 21
	s_barrier
	s_waitcnt vmcnt(9)
	v_mbcnt_lo_u32_b32 v0, -1, 0
	v_mbcnt_hi_u32_b32 v0, -1, v0
	s_nop 0
	v_cmp_eq_u32_e32 vcc, s0, v0
	s_and_saveexec_b64 s[0:1], vcc
	s_cbranch_execz .LBB0_731
	s_add_i32 s4, 0, 0x23d60
	v_mov_b32_e32 v0, s4
	s_waitcnt vmcnt(0) expcnt(0) lgkmcnt(0)
	ds_read_b32 v2, v0
	s_add_i32 s4, 0, 0x23d64
	v_mov_b32_e32 v0, s4
	ds_read_b32 v0, v0
	s_waitcnt lgkmcnt(1)
	v_cmp_ne_u32_e32 vcc, 0, v2
	s_cbranch_vccnz .LBB0_695
	v_readlane_b32 s4, v254, 0
	v_readlane_b32 s5, v254, 1
	s_load_dwordx2 s[8:9], s[4:5], 0x120
	s_load_dword s7, s[4:5], 0x128
	s_add_u32 s4, s92, 0x4200
	s_addc_u32 s5, s93, 0
	s_add_u32 s6, s92, 0x4400
	s_waitcnt lgkmcnt(0)
	s_mul_i32 s48, s9, s8
	s_mul_i32 s48, s48, s7
	s_addc_u32 s7, s93, 0
	s_add_u32 s8, s92, 0x4500
	s_addc_u32 s9, s93, 0
	s_add_u32 s10, s92, 0x4600
	s_addc_u32 s11, s93, 0
	s_add_u32 s12, s92, 0x4700
	s_addc_u32 s13, s93, 0
	s_add_u32 s14, s92, 0x4800
	s_addc_u32 s15, s93, 0
	s_add_u32 s16, s92, 0x4900
	s_addc_u32 s17, s93, 0
	s_add_u32 s18, s92, 0x4a00
	s_addc_u32 s19, s93, 0
	s_add_u32 s20, s92, 0x4b00
	s_addc_u32 s21, s93, 0
	s_add_u32 s22, s92, 0x4c00
	s_addc_u32 s23, s93, 0
	s_add_u32 s26, s92, 0x4d00
	s_addc_u32 s27, s93, 0
	s_add_u32 s28, s92, 0x4e00
	s_addc_u32 s29, s93, 0
	s_add_u32 s30, s92, 0x4f00
	s_addc_u32 s31, s93, 0
	s_add_u32 s34, s92, 0x5000
	s_addc_u32 s35, s93, 0
	s_add_u32 s36, s92, 0x5100
	s_addc_u32 s37, s93, 0
	s_add_u32 s38, s92, 0x5200
	s_addc_u32 s39, s93, 0
	s_add_u32 s40, s92, 0x5300
	s_addc_u32 s41, s93, 0
	s_mov_b32 s49, 1
	v_mov_b32_e32 v16, 0
	s_branch .LBB0_683

;     __host__ __device__ bool next(int i, Unit& u) const {
;         if (i > 0 && c < skew) return false;
;         const long L = (i == 0) ? (long)c : (long)G + (long)(i - 1) * (G - skew) + (c - skew); if (L >= nwg) return false;
;         int wgid = (int)L; { const int q = nwg / NXCD, r = nwg % NXCD, xcd = wgid % NXCD, off = wgid / NXCD; wgid = (xcd < r ? xcd * (q + 1) : r * (q + 1) + (xcd - r) * q) + off; }
;         const int nig = WGM * nN, gid = wgid / nig, fm = gid * WGM, gsz = (nM - fm) < WGM ? (nM - fm) : WGM;
;         u.pm = fm + ((wgid % nig) % gsz); u.pn = (wgid % nig) / gsz; u.pb = u.pn; u.po = u.pm; return true;
; template <class Epi, class Sched, bool ALIGN_EPI = false, bool SP2 = false, bool F8 = false, bool I8 = false, bool PF = false>
; __device__ __forceinline__ void gemm_phase(PG8_LAS unsigned char* lds, const Gemm g, const Sched& S, const Epi& E, const int wave_) {
;     ...
;     const int tid = tid_, wid = __builtin_amdgcn_readfirstlane(tid >> 6), lane = tid & 63, wr = wid >> 2, wc = wid & 3, fr = lane & 15, fq = lane >> 4;
;     const int K = g.K, nt = K / BK;
;     unsigned voffA[2], voffB[2];
; #pragma unroll
;     for (int i = 0; i < 2; ++i) { int R, C; stage_rc(tid * 16 + i * 8192, R, C); const int Rb = Epi::PERM ? ((R & ~31) + perm32(R & 31)) : R;
;         voffA[i] = (unsigned)(R * K + C) * 2u; voffB[i] = (unsigned)(Rb * K + C) * 2u; }
;     const size_t kstep = (size_t)(BK * 2);
;     const size_t hstep = (size_t)HALF * K * 2;
;     const size_t tstep = 2 * hstep;
;     const unsigned lds_a32 = (unsigned)(uintptr_t)lds;
;     const unsigned ldsw = (unsigned)wid * 1024u;
;     const int aoff = lds_byte(wr * 64 + fr, fq * 8), boff = lds_byte(wc * 32 + fr, fq * 8);
.LBB0_798:
	s_cmp_lt_i32 s94, 10
	s_cselect_b64 s[0:1], -1, 0
	s_and_b64 s[0:1], s[0:1], s[2:3]
	s_andn2_b64 vcc, exec, s[0:1]
	s_cbranch_vccnz .LBB0_816
	s_cmp_lt_u32 s96, 0x100
	s_cbranch_scc1 .Lsp_9
	s_setprio 1
.Lsp_9:
	s_waitcnt vmcnt(9)
	v_mbcnt_lo_u32_b32 v0, -1, 0
	v_mbcnt_hi_u32_b32 v0, -1, v0
	s_cmpk_gt_i32 s33, 0x4ff
	v_add_u32_e32 v0, s96, v0
	s_nop 0
	v_mbcnt_lo_u32_b32 v0, -1, 0
	v_mbcnt_hi_u32_b32 v0, -1, v0
	s_waitcnt vmcnt(7)
	v_add_u32_e32 v9, s96, v0
	s_nop 0
	v_readfirstlane_b32 s3, v9
	s_cbranch_scc1 .LBB0_816
	v_lshlrev_b32_e32 v0, 4, v9
	v_add_u32_e32 v1, 0x2000, v0
	v_ashrrev_i32_e32 v2, 31, v1
	v_lshrrev_b32_e32 v2, 22, v2
	v_add_u32_e32 v2, v1, v2
	v_ashrrev_i32_e32 v8, 10, v2
	v_mul_i32_i24_e32 v2, 0x400, v8
	v_sub_u32_e32 v1, v1, v2
	v_lshrrev_b32_e32 v2, 4, v1
	v_bitop3_b32 v1, v2, v1, 32 bitop3:0x6c
	v_ashrrev_i32_e32 v2, 31, v1
	v_lshrrev_b32_e32 v2, 26, v2
	v_add_u32_e32 v2, v1, v2
	v_lshlrev_b32_e32 v3, 3, v8
	v_ashrrev_i32_e32 v10, 6, v2
	v_and_b32_e32 v3, -16, v3
	v_add_u32_e32 v3, v10, v3
	v_and_b32_e32 v4, 3, v10
	s_mov_b32 s2, 0x3fffe0
	v_lshrrev_b32_e32 v5, 2, v3
	v_lshlrev_b32_e32 v6, 1, v3
	v_and_b32_e32 v2, 0xc0, v2
	v_and_or_b32 v4, v3, s2, v4
	v_and_b32_e32 v5, 4, v5
	v_and_b32_e32 v6, 24, v6
	v_sub_u32_e32 v1, v1, v2
	v_mov_b32_e32 v2, 1
	v_or3_b32 v4, v4, v5, v6
	v_lshlrev_b32_e32 v5, 5, v8
	v_ashrrev_i16_sdwa v1, v2, sext(v1) dst_sel:DWORD dst_unused:UNUSED_PAD src0_sel:DWORD src1_sel:BYTE_0
	v_and_b32_e32 v5, 32, v5
	v_bfe_i32 v11, v1, 0, 16
	v_add_lshl_u32 v1, v5, v11, 1
	v_lshl_add_u32 v128, v4, 10, v1
	v_lshl_add_u32 v130, v3, 10, v1
	v_bfe_i32 v1, v9, 27, 1
	v_lshrrev_b32_e32 v1, 22, v1
	v_add_u32_e32 v1, v0, v1
	v_and_b32_e32 v1, 0xfffffc00, v1
	v_sub_u32_e32 v0, v0, v1
	v_lshrrev_b32_e32 v1, 4, v0
	v_ashrrev_i32_e32 v3, 31, v9
	v_bitop3_b32 v0, v1, v0, 32 bitop3:0x6c
	v_lshrrev_b32_e32 v3, 26, v3
	v_ashrrev_i32_e32 v1, 31, v0
	v_add_u32_e32 v3, v9, v3
	v_lshrrev_b32_e32 v1, 26, v1
	s_waitcnt vmcnt(6)
	v_ashrrev_i32_e32 v13, 6, v3
	v_add_u32_e32 v1, v0, v1
	v_lshlrev_b32_e32 v3, 3, v13
	v_ashrrev_i32_e32 v12, 6, v1
	v_and_b32_e32 v3, -16, v3
	s_add_u32 s15, s92, 0x20000000
	v_add_u32_e32 v3, v12, v3
	v_and_b32_e32 v4, 3, v12
	s_addc_u32 s38, s93, 0
	v_and_or_b32 v4, v3, s2, v4
	s_ashr_i32 s2, s33, 31
	s_lshr_b32 s2, s2, 29
	s_add_i32 s2, s33, s2
	s_ashr_i32 s10, s3, 6
	s_ashr_i32 s4, s2, 3
	s_and_b32 s2, s2, -8
	s_ashr_i32 s11, s3, 8
	s_lshl_b32 s39, s10, 10
	s_sub_i32 s2, s33, s2
	s_cmp_lt_i32 s2, 0
	s_movk_i32 s40, 0xa1
	s_cselect_b32 s5, s40, 0xa0
	s_mul_i32 s2, s2, s5
	s_add_i32 s2, s2, s4
	s_mul_hi_i32 s4, s2, 0x66666667
	s_lshr_b32 s5, s4, 31
	s_ashr_i32 s4, s4, 5
	s_add_i32 s4, s4, s5
	s_lshl_b32 s5, s4, 3
	s_mulk_i32 s4, 0x50
	s_sub_i32 s4, s2, s4
	s_bfe_i32 s2, s4, 0x80000
	s_bfe_u32 s2, s2, 0x3000c
	s_add_i32 s6, s4, s2
	s_bfe_i32 s2, s6, 0x80000
	s_and_b32 s6, s6, 0xf8
	s_sub_i32 s4, s4, s6
	s_sext_i32_i16 s2, s2
	s_sext_i32_i8 s4, s4
	v_lshrrev_b32_e32 v5, 2, v3
	v_lshlrev_b32_e32 v6, 1, v3
	v_and_b32_e32 v1, 0xc0, v1
	s_lshr_b32 s2, s2, 3
	s_add_i32 s28, s5, s4
	v_and_b32_e32 v5, 4, v5
	v_and_b32_e32 v6, 24, v6
	v_sub_u32_e32 v0, v0, v1
	s_ashr_i32 s29, s28, 31
	s_bfe_i64 s[6:7], s[2:3], 0x100000
	v_or3_b32 v4, v4, v5, v6
	v_lshlrev_b32_e32 v5, 5, v13
	v_ashrrev_i16_sdwa v0, v2, sext(v0) dst_sel:DWORD dst_unused:UNUSED_PAD src0_sel:DWORD src1_sel:BYTE_0
	s_lshl_b64 s[4:5], s[28:29], 18
	s_lshl_b64 s[6:7], s[6:7], 18
	v_and_b32_e32 v5, 32, v5
	v_bfe_i32 v14, v0, 0, 16
	s_add_u32 s34, s15, s6
	v_add_lshl_u32 v0, v5, v14, 1
	s_addc_u32 s35, s38, s7
	s_add_i32 s29, s39, 0
	v_lshl_add_u32 v132, v4, 10, v0
	s_add_i32 m0, s29, 0x10000
	v_lshl_add_u32 v134, v3, 10, v0
	global_load_lds_dwordx4 v132, s[34:35]
	s_add_i32 m0, s29, 0x12000
	s_add_u32 s6, s34, 0x20000
	global_load_lds_dwordx4 v128, s[34:35]
	s_addc_u32 s7, s35, 0
	s_add_i32 m0, s29, 0x14000
	v_mov_b32_e32 v133, 0
	global_load_lds_dwordx4 v132, s[6:7]
	s_add_i32 m0, s29, 0x16000
	s_add_u32 s30, s58, s4
	s_addc_u32 s31, s59, s5
	s_add_i32 s41, s29, 0x2000
	global_load_lds_dwordx4 v128, s[6:7]
	s_mov_b32 m0, s29
	s_add_u32 s4, s30, 0x20000
	global_load_lds_dwordx4 v134, s[30:31]
	s_mov_b32 m0, s41
	s_addc_u32 s5, s31, 0
	s_add_i32 s42, s29, 0x4000
	global_load_lds_dwordx4 v130, s[30:31]
	s_mov_b32 m0, s42
	s_add_i32 s43, s29, 0x6000
	global_load_lds_dwordx4 v134, s[4:5]
	s_mov_b32 m0, s43
	v_mov_b32_e32 v129, v133
	global_load_lds_dwordx4 v130, s[4:5]
	v_readlane_b32 s4, v254, 0
	v_readlane_b32 s5, v254, 1
	s_load_dword s45, s[4:5], 0x120
	v_mov_b32_e32 v135, v133
	v_mov_b32_e32 v131, v133
	s_cmp_eq_u32 s11, 1
	s_mov_b32 s44, 0
	v_lshl_add_u64 v[6:7], s[34:35], 0, v[132:133]
	v_lshl_add_u64 v[4:5], s[34:35], 0, v[128:129]
	v_lshl_add_u64 v[0:1], s[30:31], 0, v[134:135]
	s_cselect_b64 s[4:5], -1, 0
	s_cmp_lg_u32 s11, 1
	v_lshl_add_u64 v[2:3], s[30:31], 0, v[130:131]
	s_cbranch_scc1 .LBB0_802
	s_barrier

; __device__ __forceinline__ int tid_from_wave(int wave) { unsigned l_; asm volatile("v_mbcnt_lo_u32_b32 %0, -1, 0\n\tv_mbcnt_hi_u32_b32 %0, -1, %0" : "=v"(l_)); return wave * 64 + (int)l_; }
; __device__ __forceinline__ unsigned xb_ld(unsigned* p)              { return __hip_atomic_load(p, __ATOMIC_RELAXED, __HIP_MEMORY_SCOPE_AGENT); }
; __device__ __forceinline__ unsigned xb_add(unsigned* p, unsigned v) { return __hip_atomic_fetch_add(p, v, __ATOMIC_RELAXED, __HIP_MEMORY_SCOPE_AGENT); }
; __device__ __forceinline__ void xcd_barrier_complete(unsigned* bar, unsigned x, unsigned& nloc, unsigned& nx) {
;     const unsigned G = gridDim.x * gridDim.y * gridDim.z;
;     unsigned sum, cnt, mine, sp = 0u;
;     for (;;) {
;         sum = 0u; cnt = 0u; mine = 0u;
; #pragma unroll
;         for (unsigned j = 0; j < 16; ++j) { const unsigned c = xb_ld(&bar[XB_XCNT(j)]); sum += c; cnt += (c > 0u) ? 1u : 0u; mine = (j == x) ? c : mine; }
;         if (sum == G) break;
;         __builtin_amdgcn_s_sleep(1);
;         if ((++sp & 255u) == 0u) { if (xb_ld(&bar[XB_TMO])) break; if (sp > XB_SPIN_CAP) { atomicAdd(&bar[XB_TMO], 1u); break; } }
; __device__ __forceinline__ void xcd_barrier(const XcdBarrier& b) {
;     asm volatile("s_waitcnt vmcnt(0)" ::: "memory");
;     __syncthreads();
;     if (tid_from_wave(b.wave) == 0) {
;         unsigned* bar = b.bar;
;         __builtin_amdgcn_s_waitcnt(0);
;         unsigned nloc = b.st[0], nx = b.st[1];
;         if (nloc == 0u) { xcd_barrier_complete(bar, b.x, nloc, nx); b.st[0] = nloc; b.st[1] = nx; }
;         const unsigned old = xb_add(&bar[XB_XSUB(b.x)], 1u);
.LBB0_816:
	s_setprio 0
	s_cmp_gt_i32 s95, 10
	s_cselect_b64 s[2:3], -1, 0
	s_and_b64 s[0:1], s[0:1], s[2:3]
	s_andn2_b64 vcc, exec, s[0:1]
	s_cbranch_vccnz .LBB0_870
	s_waitcnt vmcnt(0)
	v_readlane_b32 s0, v254, 21
	s_barrier
	s_waitcnt vmcnt(9)
	v_mbcnt_lo_u32_b32 v0, -1, 0
	v_mbcnt_hi_u32_b32 v0, -1, v0
	s_nop 0
	v_cmp_eq_u32_e32 vcc, s0, v0
	s_and_saveexec_b64 s[0:1], vcc
	s_cbranch_execz .LBB0_869
	s_add_i32 s4, 0, 0x23d60
	v_mov_b32_e32 v0, s4
	s_waitcnt vmcnt(0) expcnt(0) lgkmcnt(0)
	ds_read_b32 v2, v0
	s_add_i32 s4, 0, 0x23d64
	v_mov_b32_e32 v0, s4
	ds_read_b32 v0, v0
	s_waitcnt lgkmcnt(1)
	v_cmp_ne_u32_e32 vcc, 0, v2
	s_cbranch_vccnz .LBB0_833
	v_readlane_b32 s4, v254, 0
	v_readlane_b32 s5, v254, 1
	s_load_dwordx2 s[8:9], s[4:5], 0x120
	s_load_dword s7, s[4:5], 0x128
	s_add_u32 s4, s92, 0x4200
	s_addc_u32 s5, s93, 0
	s_add_u32 s6, s92, 0x4400
	s_waitcnt lgkmcnt(0)
	s_mul_i32 s48, s9, s8
	s_mul_i32 s48, s48, s7
	s_addc_u32 s7, s93, 0
	s_add_u32 s8, s92, 0x4500
	s_addc_u32 s9, s93, 0
	s_add_u32 s10, s92, 0x4600
	s_addc_u32 s11, s93, 0
	s_add_u32 s12, s92, 0x4700
	s_addc_u32 s13, s93, 0
	s_add_u32 s14, s92, 0x4800
	s_addc_u32 s15, s93, 0
	s_add_u32 s16, s92, 0x4900
	s_addc_u32 s17, s93, 0
	s_add_u32 s18, s92, 0x4a00
	s_addc_u32 s19, s93, 0
	s_add_u32 s20, s92, 0x4b00
	s_addc_u32 s21, s93, 0
	s_add_u32 s22, s92, 0x4c00
	s_addc_u32 s23, s93, 0
	s_add_u32 s26, s92, 0x4d00
	s_addc_u32 s27, s93, 0
	s_add_u32 s28, s92, 0x4e00
	s_addc_u32 s29, s93, 0
	s_add_u32 s30, s92, 0x4f00
	s_addc_u32 s31, s93, 0
	s_add_u32 s34, s92, 0x5000
	s_addc_u32 s35, s93, 0
	s_add_u32 s36, s92, 0x5100
	s_addc_u32 s37, s93, 0
	s_add_u32 s38, s92, 0x5200
	s_addc_u32 s39, s93, 0
	s_add_u32 s40, s92, 0x5300
	s_addc_u32 s41, s93, 0
	s_mov_b32 s49, 1
	v_mov_b32_e32 v16, 0
	s_branch .LBB0_821

; #define MKCTX() Ctx C; { int t_ = tid_from_wave(wave_s); asm volatile("" : "+v"(t_)); C.lds = (LAS unsigned char*)lds_raw; C.tid = t_; C.lane = t_ & 63; C.wave = __builtin_amdgcn_readfirstlane(t_ >> 6); \
;         C.G = gridDim.x; const int bx_ = blockIdx.x; C.vcu = (C.G % 8 == 0) ? (bx_ % 8) * (C.G / 8) + bx_ / 8 : bx_; C.gw = C.vcu * NWAVES + C.wave; C.NGW = C.G * NWAVES; }
;     __host__ __device__ bool next(int i, Unit& u) const {
;         if (i > 0 && c < skew) return false;
;         const long L = (i == 0) ? (long)c : (long)G + (long)(i - 1) * (G - skew) + (c - skew); if (L >= nwg) return false;
;         int wgid = (int)L; { const int q = nwg / NXCD, r = nwg % NXCD, xcd = wgid % NXCD, off = wgid / NXCD; wgid = (xcd < r ? xcd * (q + 1) : r * (q + 1) + (xcd - r) * q) + off; }
;         const int nig = WGM * nN, gid = wgid / nig, fm = gid * WGM, gsz = (nM - fm) < WGM ? (nM - fm) : WGM;
;         u.pm = fm + ((wgid % nig) % gsz); u.pn = (wgid % nig) / gsz; u.pb = u.pn; u.po = u.pm; return true;
; __global__ void __launch_bounds__(NWAVES * 64, 2) fwd(Args args) {
;     ...
;     if (IN(11)) for (int rep_ = 0; rep_ < NREP(11); ++rep_) { MKCTX();
;         { pg8::Gemm g{QN, (const bf16*)(ws + WS_WQB), NTOK, 768, 512}; pg8::StaticOrder S; S.init(NTOK, 768, C.G, (int)blockIdx.x);
;           pg8::EpiQRope E{Q, 768, ctab, stab, QS_ODD, SEQ - 1}; pg8::gemm_phase<pg8::EpiQRope, pg8::StaticOrder, true, true>(C.lds, g, S, E, wave_s); }
;         { pg8::Gemm g{KVN, (const bf16*)(ws + WS_WKVB), NTOK, 1024, 256}; pg8::StaticOrder S; S.init(NTOK, 1024, C.G, (int)blockIdx.x, (C.G == 256) ? 128 : 0);
.LBB0_954:
	s_cmp_lt_i32 s94, 12
	s_cselect_b64 s[0:1], -1, 0
	s_add_u32 s6, s92, 0x10800000
	s_addc_u32 s7, s93, 0
	s_and_b64 s[12:13], s[0:1], s[2:3]
	s_andn2_b64 vcc, exec, s[12:13]
	s_cbranch_vccnz .LBB0_1025
	s_cmp_lt_u32 s96, 0x100
	s_cbranch_scc1 .Lsp_11
	s_setprio 1
.Lsp_11:
	s_cmpk_lt_i32 s33, 0x180
	s_cselect_b64 s[2:3], -1, 0
	s_ashr_i32 s0, s33, 31
	s_lshr_b32 s0, s0, 29
	s_add_i32 s0, s33, s0
	s_waitcnt vmcnt(9)
	v_mbcnt_lo_u32_b32 v0, -1, 0
	v_mbcnt_hi_u32_b32 v0, -1, v0
	s_ashr_i32 s44, s0, 3
	s_and_b32 s0, s0, -8
	v_add_u32_e32 v0, s96, v0
	s_sub_i32 s45, s33, s0
	s_cmp_lt_i32 s45, 0
	v_mbcnt_lo_u32_b32 v0, -1, 0
	v_mbcnt_hi_u32_b32 v0, -1, v0
	s_cselect_b64 s[0:1], -1, 0
	s_waitcnt vmcnt(7)
	v_add_u32_e32 v8, s96, v0
	s_cmpk_gt_i32 s33, 0x17f
	s_nop 0
	v_readfirstlane_b32 s18, v8
	s_cbranch_scc1 .LBB0_957
	s_and_b64 s[4:5], s[0:1], exec
	s_cselect_b32 s4, 49, 48
	s_mul_i32 s4, s45, s4
	s_add_i32 s4, s4, s44
	s_mul_hi_i32 s5, s4, 0x2aaaaaab
	s_lshr_b32 s14, s5, 31
	s_ashr_i32 s5, s5, 2
	s_add_i32 s5, s5, s14
	s_lshl_b32 s14, s5, 3
	s_mul_i32 s5, s5, 24
	s_sub_i32 s4, s4, s5
	s_bfe_i32 s5, s4, 0x80000
	s_bfe_u32 s5, s5, 0x3000c
	s_add_i32 s5, s4, s5
	s_bfe_i32 s15, s5, 0x80000
	s_and_b32 s5, s5, 0xf8
	s_sub_i32 s4, s4, s5
	s_sext_i32_i16 s15, s15
	s_sext_i32_i8 s4, s4
	s_add_i32 s4, s14, s4
	s_ashr_i32 s36, s15, 3

; __device__ __forceinline__ int tid_from_wave(int wave) { unsigned l_; asm volatile("v_mbcnt_lo_u32_b32 %0, -1, 0\n\tv_mbcnt_hi_u32_b32 %0, -1, %0" : "=v"(l_)); return wave * 64 + (int)l_; }
; __device__ __forceinline__ unsigned xb_ld(unsigned* p)              { return __hip_atomic_load(p, __ATOMIC_RELAXED, __HIP_MEMORY_SCOPE_AGENT); }
; __device__ __forceinline__ unsigned xb_add(unsigned* p, unsigned v) { return __hip_atomic_fetch_add(p, v, __ATOMIC_RELAXED, __HIP_MEMORY_SCOPE_AGENT); }
; __device__ __forceinline__ void xcd_barrier_complete(unsigned* bar, unsigned x, unsigned& nloc, unsigned& nx) {
;     const unsigned G = gridDim.x * gridDim.y * gridDim.z;
;     unsigned sum, cnt, mine, sp = 0u;
;     for (;;) {
;         sum = 0u; cnt = 0u; mine = 0u;
; #pragma unroll
;         for (unsigned j = 0; j < 16; ++j) { const unsigned c = xb_ld(&bar[XB_XCNT(j)]); sum += c; cnt += (c > 0u) ? 1u : 0u; mine = (j == x) ? c : mine; }
;         if (sum == G) break;
;         __builtin_amdgcn_s_sleep(1);
;         if ((++sp & 255u) == 0u) { if (xb_ld(&bar[XB_TMO])) break; if (sp > XB_SPIN_CAP) { atomicAdd(&bar[XB_TMO], 1u); break; } }
; __device__ __forceinline__ void xcd_barrier(const XcdBarrier& b) {
;     asm volatile("s_waitcnt vmcnt(0)" ::: "memory");
;     __syncthreads();
;     if (tid_from_wave(b.wave) == 0) {
;         unsigned* bar = b.bar;
;         __builtin_amdgcn_s_waitcnt(0);
;         unsigned nloc = b.st[0], nx = b.st[1];
;         if (nloc == 0u) { xcd_barrier_complete(bar, b.x, nloc, nx); b.st[0] = nloc; b.st[1] = nx; }
;         const unsigned old = xb_add(&bar[XB_XSUB(b.x)], 1u);
.LBB0_1025:
	s_setprio 0
	s_cmp_gt_i32 s95, 12
	s_cselect_b64 s[0:1], -1, 0
	s_and_b64 s[2:3], s[12:13], s[0:1]
	s_andn2_b64 vcc, exec, s[2:3]
	s_cbranch_vccnz .LBB0_1079
	s_waitcnt vmcnt(0)
	v_readlane_b32 s2, v254, 21
	s_waitcnt vmcnt(0) lgkmcnt(0)
	s_barrier
	v_mbcnt_lo_u32_b32 v0, -1, 0
	v_mbcnt_hi_u32_b32 v0, -1, v0
	s_nop 0
	v_cmp_eq_u32_e32 vcc, s2, v0
	s_and_saveexec_b64 s[2:3], vcc
	s_cbranch_execz .LBB0_1078
	s_add_i32 s4, 0, 0x23d60
	v_mov_b32_e32 v0, s4
	s_waitcnt vmcnt(0) expcnt(0) lgkmcnt(0)
	ds_read_b32 v2, v0
	s_add_i32 s4, 0, 0x23d64
	v_mov_b32_e32 v0, s4
	ds_read_b32 v0, v0
	s_waitcnt lgkmcnt(1)
	v_cmp_ne_u32_e32 vcc, 0, v2
	s_cbranch_vccnz .LBB0_1042
	v_readlane_b32 s4, v254, 0
	v_readlane_b32 s5, v254, 1
	s_load_dwordx2 s[10:11], s[4:5], 0x120
	s_load_dword s9, s[4:5], 0x128
	s_add_u32 s4, s92, 0x4200
	s_addc_u32 s5, s93, 0
	s_add_u32 s8, s92, 0x4400
	s_waitcnt lgkmcnt(0)
	s_mul_i32 s50, s11, s10
	s_mul_i32 s50, s50, s9
	s_addc_u32 s9, s93, 0
	s_add_u32 s10, s92, 0x4500
	s_addc_u32 s11, s93, 0
	s_add_u32 s12, s92, 0x4600
	s_addc_u32 s13, s93, 0
	s_add_u32 s14, s92, 0x4700
	s_addc_u32 s15, s93, 0
	s_add_u32 s16, s92, 0x4800
	s_addc_u32 s17, s93, 0
	s_add_u32 s18, s92, 0x4900
	s_addc_u32 s19, s93, 0
	s_add_u32 s20, s92, 0x4a00
	s_addc_u32 s21, s93, 0
	s_add_u32 s22, s92, 0x4b00
	s_addc_u32 s23, s93, 0
	s_add_u32 s26, s92, 0x4c00
	s_addc_u32 s27, s93, 0
	s_add_u32 s28, s92, 0x4d00
	s_addc_u32 s29, s93, 0
	s_add_u32 s30, s92, 0x4e00
	s_addc_u32 s31, s93, 0
	s_add_u32 s34, s92, 0x4f00
	s_addc_u32 s35, s93, 0
	s_add_u32 s36, s92, 0x5000
	s_addc_u32 s37, s93, 0
	s_add_u32 s38, s92, 0x5100
	s_addc_u32 s39, s93, 0
	s_add_u32 s40, s92, 0x5200
	s_addc_u32 s41, s93, 0
	s_add_u32 s42, s92, 0x5300
	s_addc_u32 s43, s93, 0
	s_mov_b32 s51, 1
	v_mov_b32_e32 v16, 0
	s_branch .LBB0_1030

; #define PG8_WAIT_V(n) asm volatile("s_waitcnt vmcnt(" #n ")" ::: "memory")
; #define PG8_BAR __builtin_amdgcn_s_barrier()
; template <class Epi, class Sched, bool ALIGN_EPI = false, bool SP2 = false, bool F8 = false, bool I8 = false, bool PF = false>
; __device__ __forceinline__ void gemm_phase(PG8_LAS unsigned char* lds, const Gemm g, const Sched& S, const Epi& E, const int wave_) {
;     ...
;     const int tid = tid_, wid = __builtin_amdgcn_readfirstlane(tid >> 6), lane = tid & 63, wr = wid >> 2, wc = wid & 3, fr = lane & 15, fq = lane >> 4;
;     const int K = g.K, nt = K / BK;
;     unsigned voffA[2], voffB[2];
; #pragma unroll
;     for (int i = 0; i < 2; ++i) { int R, C; stage_rc(tid * 16 + i * 8192, R, C); const int Rb = Epi::PERM ? ((R & ~31) + perm32(R & 31)) : R;
;         voffA[i] = (unsigned)(R * K + C) * 2u; voffB[i] = (unsigned)(Rb * K + C) * 2u; }
;     const size_t kstep = (size_t)(BK * 2);
;     const size_t hstep = (size_t)HALF * K * 2;
;     const size_t tstep = 2 * hstep;
;     const unsigned lds_a32 = (unsigned)(uintptr_t)lds;
;     const unsigned ldsw = (unsigned)wid * 1024u;
;     const int aoff = lds_byte(wr * 64 + fr, fq * 8), boff = lds_byte(wc * 32 + fr, fq * 8);
;     ...
;     const char* cA = (const char*)g.A + (size_t)cur.pm * tstep; const char* cB = (const char*)g.Bt + (size_t)cur.pb * tstep;
;     S.a_ready(cur);
;     if constexpr (PF) {
;         PG8_STAGE(PG8_SA(0, 0), cA, voffA); PG8_STAGE(PG8_SB(0, 0), cB, voffB); PG8_STAGE(PG8_SA(0, 1), cA + hstep, voffA); PG8_STAGE(PG8_SB(0, 1), cB + hstep, voffB);
;         PG8_STAGE(PG8_SA(1, 0), cA + kstep, voffA); PG8_STAGE(PG8_SB(1, 0), cB + kstep, voffB);
;         if (wr == 1) { PG8_STAGE(PG8_SA(1, 1), cA + hstep + kstep, voffA); PG8_STAGE(PG8_SB(1, 1), cB + hstep + kstep, voffB); }
;         PG8_WAIT_V(8); PG8_BAR;
;         PG8_LDA(At, 0, 0); PG8_LDB(B0, 0, 0); __builtin_amdgcn_s_waitcnt(0xC07F);
;         if (wr == 1) PG8_BAR;
;     } else
;     if constexpr (SP2) {
;         PG8_STAGE(PG8_SB(0, 0), cB, voffB); PG8_STAGE(PG8_SB(0, 1), cB + hstep, voffB); PG8_STAGE(PG8_SA(0, 0), cA, voffA); PG8_STAGE(PG8_SA(0, 1), cA + hstep, voffA);
;         if (wr == 1) PG8_BAR;
;         PG8_WAIT_V(2); PG8_BAR;
;         PG8_STAGE(PG8_SB(1, 0), cB + kstep, voffB); PG8_STAGE(PG8_SA(1, 0), cA + kstep, voffA); PG8_STAGE(PG8_SB(1, 1), cB + hstep + kstep, voffB);
;         PG8_WAIT_V(6); PG8_BAR;
.LBB0_1289:
	s_cmp_lt_i32 s94, 14
	s_cselect_b64 s[2:3], -1, 0
	s_and_b64 s[0:1], s[2:3], s[0:1]
	s_andn2_b64 vcc, exec, s[0:1]
	s_cbranch_vccnz .LBB0_1311
	s_cmp_lt_u32 s96, 0x100
	s_cbranch_scc1 .Lsp_13
	s_setprio 1
.Lsp_13:
	s_waitcnt vmcnt(0)
	v_mbcnt_lo_u32_b32 v0, -1, 0
	v_mbcnt_hi_u32_b32 v0, -1, v0
	s_cmpk_gt_i32 s33, 0x1ff
	v_add_u32_e32 v0, s96, v0
	s_nop 0
	v_mbcnt_lo_u32_b32 v0, -1, 0
	v_mbcnt_hi_u32_b32 v0, -1, v0
	s_nop 0
	v_add_u32_e32 v9, s96, v0
	s_nop 0
	v_readfirstlane_b32 s3, v9
	s_cbranch_scc1 .LBB0_1311
	v_lshlrev_b32_e32 v0, 4, v9
	v_add_u32_e32 v1, 0x2000, v0
	v_ashrrev_i32_e32 v2, 31, v1
	v_lshrrev_b32_e32 v2, 22, v2
	v_add_u32_e32 v2, v1, v2
	v_ashrrev_i32_e32 v8, 10, v2
	v_mul_i32_i24_e32 v2, 0x400, v8
	v_sub_u32_e32 v1, v1, v2
	v_lshrrev_b32_e32 v2, 4, v1
	v_bitop3_b32 v1, v2, v1, 32 bitop3:0x6c
	v_ashrrev_i32_e32 v2, 31, v1
	v_lshrrev_b32_e32 v2, 26, v2
	v_add_u32_e32 v2, v1, v2
	v_lshlrev_b32_e32 v3, 3, v8
	v_ashrrev_i32_e32 v10, 6, v2
	v_and_b32_e32 v3, -16, v3
	v_add_u32_e32 v3, v10, v3
	v_and_b32_e32 v4, 3, v10
	s_mov_b32 s2, 0x1fffe0
	v_lshrrev_b32_e32 v5, 2, v3
	v_lshlrev_b32_e32 v6, 1, v3
	v_and_b32_e32 v2, 0xc0, v2
	v_and_or_b32 v4, v3, s2, v4
	v_and_b32_e32 v5, 4, v5
	v_and_b32_e32 v6, 24, v6
	v_sub_u32_e32 v1, v1, v2
	v_mov_b32_e32 v2, 1
	v_or3_b32 v4, v4, v5, v6
	v_lshlrev_b32_e32 v5, 5, v8
	v_ashrrev_i16_sdwa v1, v2, sext(v1) dst_sel:DWORD dst_unused:UNUSED_PAD src0_sel:DWORD src1_sel:BYTE_0
	v_and_b32_e32 v5, 32, v5
	v_bfe_i32 v11, v1, 0, 16
	v_add_lshl_u32 v1, v5, v11, 1
	v_lshl_add_u32 v180, v4, 11, v1
	v_lshl_add_u32 v182, v3, 11, v1
	v_bfe_i32 v1, v9, 27, 1
	v_lshrrev_b32_e32 v1, 22, v1
	v_add_u32_e32 v1, v0, v1
	v_and_b32_e32 v1, 0xfffffc00, v1
	v_sub_u32_e32 v0, v0, v1
	v_lshrrev_b32_e32 v1, 4, v0
	v_ashrrev_i32_e32 v3, 31, v9
	v_bitop3_b32 v0, v1, v0, 32 bitop3:0x6c
	v_lshrrev_b32_e32 v3, 26, v3
	v_ashrrev_i32_e32 v1, 31, v0
	v_add_u32_e32 v3, v9, v3
	v_lshrrev_b32_e32 v1, 26, v1
	v_ashrrev_i32_e32 v13, 6, v3
	v_add_u32_e32 v1, v0, v1
	v_lshlrev_b32_e32 v3, 3, v13
	v_ashrrev_i32_e32 v12, 6, v1
	v_and_b32_e32 v3, -16, v3
	s_add_u32 s38, s92, 0x20640000
	v_add_u32_e32 v3, v12, v3
	v_and_b32_e32 v4, 3, v12
	s_addc_u32 s39, s93, 0
	v_and_or_b32 v4, v3, s2, v4
	s_ashr_i32 s2, s33, 31
	s_lshr_b32 s2, s2, 29
	s_add_i32 s2, s33, s2
	s_ashr_i32 s4, s2, 3
	s_and_b32 s2, s2, -8
	s_ashr_i32 s8, s3, 6
	s_sub_i32 s2, s33, s2
	s_ashr_i32 s9, s3, 8
	s_lshl_b32 s40, s8, 10
	s_lshl_b32 s6, s2, 6
	s_mul_i32 s5, s2, 0x41
	s_cmp_lt_i32 s2, 0
	s_cselect_b32 s2, s5, s6
	s_add_i32 s2, s2, s4
	s_ashr_i32 s4, s2, 31
	s_lshr_b32 s4, s4, 27
	s_add_i32 s4, s2, s4
	s_ashr_i32 s5, s4, 5
	s_and_b32 s4, s4, 0xffe0
	s_sub_i32 s4, s2, s4
	s_bfe_i32 s2, s4, 0x80000
	s_bfe_u32 s2, s2, 0x3000c
	s_add_i32 s6, s4, s2
	s_bfe_i32 s2, s6, 0x80000
	s_and_b32 s6, s6, 0xf8
	s_sub_i32 s4, s4, s6
	s_lshl_b32 s5, s5, 3
	s_sext_i32_i16 s2, s2
	s_sext_i32_i8 s4, s4
	v_lshrrev_b32_e32 v5, 2, v3
	v_lshlrev_b32_e32 v6, 1, v3
	v_and_b32_e32 v1, 0xc0, v1
	s_lshr_b32 s2, s2, 3
	s_add_i32 s28, s5, s4
	v_and_b32_e32 v5, 4, v5
	v_and_b32_e32 v6, 24, v6
	v_sub_u32_e32 v0, v0, v1
	s_ashr_i32 s29, s28, 31
	s_bfe_i64 s[6:7], s[2:3], 0x100000
	v_or3_b32 v4, v4, v5, v6
	v_lshlrev_b32_e32 v5, 5, v13
	v_ashrrev_i16_sdwa v0, v2, sext(v0) dst_sel:DWORD dst_unused:UNUSED_PAD src0_sel:DWORD src1_sel:BYTE_0
	s_lshl_b64 s[4:5], s[28:29], 19
	s_lshl_b64 s[6:7], s[6:7], 19
	v_and_b32_e32 v5, 32, v5
	v_bfe_i32 v14, v0, 0, 16
	s_add_u32 s34, s38, s6
	v_add_lshl_u32 v0, v5, v14, 1
	s_addc_u32 s35, s39, s7
	s_add_i32 s29, s40, 0
	v_lshl_add_u32 v184, v4, 11, v0
	s_add_i32 m0, s29, 0x10000
	v_lshl_add_u32 v186, v3, 11, v0
	global_load_lds_dwordx4 v184, s[34:35]
	s_add_i32 m0, s29, 0x12000
	s_add_u32 s6, s34, 0x40000
	global_load_lds_dwordx4 v180, s[34:35]
	s_addc_u32 s7, s35, 0
	s_add_i32 m0, s29, 0x14000
	v_mov_b32_e32 v185, 0
	global_load_lds_dwordx4 v184, s[6:7]
	s_add_i32 m0, s29, 0x16000
	s_add_u32 s30, s48, s4
	s_addc_u32 s31, s49, s5
	s_add_i32 s41, s29, 0x2000
	global_load_lds_dwordx4 v180, s[6:7]
	s_mov_b32 m0, s29
	s_add_u32 s4, s30, 0x40000
	global_load_lds_dwordx4 v186, s[30:31]
	s_mov_b32 m0, s41
	s_addc_u32 s5, s31, 0
	s_add_i32 s42, s29, 0x4000
	global_load_lds_dwordx4 v182, s[30:31]
	s_mov_b32 m0, s42
	s_add_i32 s43, s29, 0x6000
	global_load_lds_dwordx4 v186, s[4:5]
	s_mov_b32 m0, s43
	v_mov_b32_e32 v181, v185
	global_load_lds_dwordx4 v182, s[4:5]
	v_readlane_b32 s4, v254, 0
	v_readlane_b32 s5, v254, 1
	s_load_dword s45, s[4:5], 0x120
	v_mov_b32_e32 v187, v185
	v_mov_b32_e32 v183, v185
	s_cmp_eq_u32 s9, 1
	s_mov_b32 s44, 0
	v_lshl_add_u64 v[6:7], s[34:35], 0, v[184:185]
	v_lshl_add_u64 v[2:3], s[34:35], 0, v[180:181]
	s_mov_b64 s[4:5], 0x40000
	v_lshl_add_u64 v[0:1], s[30:31], 0, v[186:187]
	s_cselect_b64 s[6:7], -1, 0
	s_cmp_lg_u32 s9, 1
	v_lshl_add_u64 v[4:5], s[30:31], 0, v[182:183]
	s_cbranch_scc1 .LBB0_1293
	s_barrier

; __device__ __forceinline__ int tid_from_wave(int wave) { unsigned l_; asm volatile("v_mbcnt_lo_u32_b32 %0, -1, 0\n\tv_mbcnt_hi_u32_b32 %0, -1, %0" : "=v"(l_)); return wave * 64 + (int)l_; }
; __device__ __forceinline__ unsigned xb_ld(unsigned* p)              { return __hip_atomic_load(p, __ATOMIC_RELAXED, __HIP_MEMORY_SCOPE_AGENT); }
; __device__ __forceinline__ unsigned xb_add(unsigned* p, unsigned v) { return __hip_atomic_fetch_add(p, v, __ATOMIC_RELAXED, __HIP_MEMORY_SCOPE_AGENT); }
; __device__ __forceinline__ void xcd_barrier_complete(unsigned* bar, unsigned x, unsigned& nloc, unsigned& nx) {
;     const unsigned G = gridDim.x * gridDim.y * gridDim.z;
;     unsigned sum, cnt, mine, sp = 0u;
;     for (;;) {
;         sum = 0u; cnt = 0u; mine = 0u;
; #pragma unroll
;         for (unsigned j = 0; j < 16; ++j) { const unsigned c = xb_ld(&bar[XB_XCNT(j)]); sum += c; cnt += (c > 0u) ? 1u : 0u; mine = (j == x) ? c : mine; }
;         if (sum == G) break;
; __device__ __forceinline__ void xcd_barrier(const XcdBarrier& b) {
;     asm volatile("s_waitcnt vmcnt(0)" ::: "memory");
;     __syncthreads();
;     if (tid_from_wave(b.wave) == 0) {
;         unsigned* bar = b.bar;
;         __builtin_amdgcn_s_waitcnt(0);
;         unsigned nloc = b.st[0], nx = b.st[1];
;         if (nloc == 0u) { xcd_barrier_complete(bar, b.x, nloc, nx); b.st[0] = nloc; b.st[1] = nx; }
;         const unsigned old = xb_add(&bar[XB_XSUB(b.x)], 1u);
.LBB0_1311:
	s_setprio 0
	s_cmp_gt_i32 s95, 14
	s_cselect_b64 s[2:3], -1, 0
	s_and_b64 s[0:1], s[0:1], s[2:3]
	s_andn2_b64 vcc, exec, s[0:1]
	s_cbranch_vccnz .LBB0_1365
	s_waitcnt vmcnt(0)
	v_readlane_b32 s0, v254, 21
	s_waitcnt vmcnt(0) lgkmcnt(0)
	s_barrier
	v_mbcnt_lo_u32_b32 v0, -1, 0
	v_mbcnt_hi_u32_b32 v0, -1, v0
	s_nop 0
	v_cmp_eq_u32_e32 vcc, s0, v0
	s_and_saveexec_b64 s[0:1], vcc
	s_cbranch_execz .LBB0_1364
	s_add_i32 s4, 0, 0x23d60
	v_mov_b32_e32 v0, s4
	s_waitcnt vmcnt(0) expcnt(0) lgkmcnt(0)
	ds_read_b32 v2, v0
	s_add_i32 s4, 0, 0x23d64
	v_mov_b32_e32 v0, s4
	ds_read_b32 v0, v0
	s_waitcnt lgkmcnt(1)
	v_cmp_ne_u32_e32 vcc, 0, v2
	s_cbranch_vccnz .LBB0_1328
	v_readlane_b32 s4, v254, 0
	v_readlane_b32 s5, v254, 1
	s_load_dwordx2 s[8:9], s[4:5], 0x120
	s_load_dword s7, s[4:5], 0x128
	s_add_u32 s4, s92, 0x4200
	s_addc_u32 s5, s93, 0
	s_add_u32 s6, s92, 0x4400
	s_waitcnt lgkmcnt(0)
	s_mul_i32 s46, s9, s8
	s_mul_i32 s46, s46, s7
	s_addc_u32 s7, s93, 0
	s_add_u32 s8, s92, 0x4500
	s_addc_u32 s9, s93, 0
	s_add_u32 s10, s92, 0x4600
	s_addc_u32 s11, s93, 0
	s_add_u32 s12, s92, 0x4700
	s_addc_u32 s13, s93, 0
	s_add_u32 s14, s92, 0x4800
	s_addc_u32 s15, s93, 0
	s_add_u32 s16, s92, 0x4900
	s_addc_u32 s17, s93, 0
	s_add_u32 s18, s92, 0x4a00
	s_addc_u32 s19, s93, 0
	s_add_u32 s20, s92, 0x4b00
	s_addc_u32 s21, s93, 0
	s_add_u32 s22, s92, 0x4c00
	s_addc_u32 s23, s93, 0
	s_add_u32 s24, s92, 0x4d00
	s_addc_u32 s25, s93, 0
	s_add_u32 s26, s92, 0x4e00
	s_addc_u32 s27, s93, 0
	s_add_u32 s28, s92, 0x4f00
	s_addc_u32 s29, s93, 0
	s_add_u32 s30, s92, 0x5000
	s_addc_u32 s31, s93, 0
	s_add_u32 s34, s92, 0x5100
	s_addc_u32 s35, s93, 0
	s_add_u32 s36, s92, 0x5200
	s_addc_u32 s37, s93, 0
	s_add_u32 s38, s92, 0x5300
	s_addc_u32 s39, s93, 0
	s_mov_b32 s47, 1
	v_mov_b32_e32 v16, 0
	s_branch .LBB0_1316

; #define MKCTX() Ctx C; { int t_ = tid_from_wave(wave_s); asm volatile("" : "+v"(t_)); C.lds = (LAS unsigned char*)lds_raw; C.tid = t_; C.lane = t_ & 63; C.wave = __builtin_amdgcn_readfirstlane(t_ >> 6); \
;         C.G = gridDim.x; const int bx_ = blockIdx.x; C.vcu = (C.G % 8 == 0) ? (bx_ % 8) * (C.G / 8) + bx_ / 8 : bx_; C.gw = C.vcu * NWAVES + C.wave; C.NGW = C.G * NWAVES; }
; __global__ void __launch_bounds__(NWAVES * 64, 2) fwd(Args args) {
;     ...
;     if (IN(16)) for (int rep_ = 0; rep_ < NREP(16); ++rep_) { MKCTX();
;         const int P = __builtin_amdgcn_readfirstlane(pexp[272]);
;         pg8::MoeOrder<28, false> S{C.G, C.vcu, 0, P * 28, pexp, 0};
;         pg8::Gemm g{(const bf16*)XS, (const bf16*)(ws + WS_WEGU), 0, 0, DM / 2};
.LBB0_1505:
	s_cmp_lt_i32 s94, 17
	s_cselect_b64 s[2:3], -1, 0
	s_add_u32 s4, s92, 0x11c00000
	s_addc_u32 s5, s93, 0
	s_and_b64 s[0:1], s[2:3], s[0:1]
	s_andn2_b64 vcc, exec, s[0:1]
	s_cbranch_vccnz .LBB0_1547
	s_cmp_lt_u32 s96, 0x100
	s_cbranch_scc1 .Lsp_16
	s_setprio 1
.Lsp_16:
	s_waitcnt vmcnt(0)
	v_mbcnt_lo_u32_b32 v0, -1, 0
	v_mbcnt_hi_u32_b32 v0, -1, v0
	v_readlane_b32 s2, v254, 0
	v_add_u32_e32 v0, s96, v0
	v_readlane_b32 s3, v254, 1
	s_load_dword s13, s[2:3], 0x120
	s_mov_b32 s15, s33
	s_waitcnt lgkmcnt(0)
	s_and_b32 s2, s13, 7
	s_cmp_lg_u32 s2, 0
	s_cbranch_scc1 .LBB0_1508
	s_ashr_i32 s2, s33, 31
	s_lshr_b32 s2, s2, 29
	s_add_i32 s2, s33, s2
	s_ashr_i32 s3, s2, 3
	s_and_b32 s2, s2, -8
	s_sub_i32 s2, s33, s2
	s_ashr_i32 s6, s13, 3
	s_mul_i32 s2, s6, s2
	s_add_i32 s15, s2, s3

; __device__ __forceinline__ int tid_from_wave(int wave) { unsigned l_; asm volatile("v_mbcnt_lo_u32_b32 %0, -1, 0\n\tv_mbcnt_hi_u32_b32 %0, -1, %0" : "=v"(l_)); return wave * 64 + (int)l_; }
; __device__ __forceinline__ unsigned xb_ld(unsigned* p)              { return __hip_atomic_load(p, __ATOMIC_RELAXED, __HIP_MEMORY_SCOPE_AGENT); }
; __device__ __forceinline__ unsigned xb_add(unsigned* p, unsigned v) { return __hip_atomic_fetch_add(p, v, __ATOMIC_RELAXED, __HIP_MEMORY_SCOPE_AGENT); }
; __device__ __forceinline__ void xcd_barrier_complete(unsigned* bar, unsigned x, unsigned& nloc, unsigned& nx) {
;     const unsigned G = gridDim.x * gridDim.y * gridDim.z;
;     unsigned sum, cnt, mine, sp = 0u;
;     for (;;) {
;         sum = 0u; cnt = 0u; mine = 0u;
; #pragma unroll
;         for (unsigned j = 0; j < 16; ++j) { const unsigned c = xb_ld(&bar[XB_XCNT(j)]); sum += c; cnt += (c > 0u) ? 1u : 0u; mine = (j == x) ? c : mine; }
;         if (sum == G) break;
; __device__ __forceinline__ void xcd_barrier(const XcdBarrier& b) {
;     asm volatile("s_waitcnt vmcnt(0)" ::: "memory");
;     __syncthreads();
;     if (tid_from_wave(b.wave) == 0) {
;         unsigned* bar = b.bar;
;         __builtin_amdgcn_s_waitcnt(0);
;         unsigned nloc = b.st[0], nx = b.st[1];
;         if (nloc == 0u) { xcd_barrier_complete(bar, b.x, nloc, nx); b.st[0] = nloc; b.st[1] = nx; }
;         const unsigned old = xb_add(&bar[XB_XSUB(b.x)], 1u);
.LBB0_1547:
	s_setprio 0
	s_cmp_gt_i32 s95, 17
	s_cselect_b64 s[2:3], -1, 0
	s_and_b64 s[0:1], s[0:1], s[2:3]
	s_andn2_b64 vcc, exec, s[0:1]
	s_cbranch_vccnz .LBB0_1605
	s_waitcnt vmcnt(0)
	v_readlane_b32 s0, v254, 21
	s_waitcnt vmcnt(0) lgkmcnt(0)
	s_barrier
	v_mbcnt_lo_u32_b32 v0, -1, 0
	v_mbcnt_hi_u32_b32 v0, -1, v0
	s_nop 0
	v_cmp_eq_u32_e32 vcc, s0, v0
	s_and_saveexec_b64 s[0:1], vcc
	s_cbranch_execz .LBB0_1604
	s_add_i32 s6, 0, 0x23d60
	v_mov_b32_e32 v0, s6
	s_waitcnt vmcnt(0) expcnt(0) lgkmcnt(0)
	ds_read_b32 v2, v0
	s_add_i32 s6, 0, 0x23d64
	v_mov_b32_e32 v0, s6
	ds_read_b32 v0, v0
	s_waitcnt lgkmcnt(1)
	v_cmp_ne_u32_e32 vcc, 0, v2
	s_cbranch_vccnz .LBB0_1564
	v_readlane_b32 s6, v254, 0
	v_readlane_b32 s7, v254, 1
	s_load_dwordx2 s[10:11], s[6:7], 0x120
	s_load_dword s9, s[6:7], 0x128
	s_add_u32 s6, s92, 0x4200
	s_addc_u32 s7, s93, 0
	s_add_u32 s8, s92, 0x4400
	s_waitcnt lgkmcnt(0)
	s_mul_i32 s48, s11, s10
	s_mul_i32 s48, s48, s9
	s_addc_u32 s9, s93, 0
	s_add_u32 s10, s92, 0x4500
	s_addc_u32 s11, s93, 0
	s_add_u32 s12, s92, 0x4600
	s_addc_u32 s13, s93, 0
	s_add_u32 s14, s92, 0x4700
	s_addc_u32 s15, s93, 0
	s_add_u32 s16, s92, 0x4800
	s_addc_u32 s17, s93, 0
	s_add_u32 s18, s92, 0x4900
	s_addc_u32 s19, s93, 0
	s_add_u32 s20, s92, 0x4a00
	s_addc_u32 s21, s93, 0
	s_add_u32 s22, s92, 0x4b00
	s_addc_u32 s23, s93, 0
	s_add_u32 s24, s92, 0x4c00
	s_addc_u32 s25, s93, 0
	s_add_u32 s26, s92, 0x4d00
	s_addc_u32 s27, s93, 0
	s_add_u32 s28, s92, 0x4e00
	s_addc_u32 s29, s93, 0
	s_add_u32 s30, s92, 0x4f00
	s_addc_u32 s31, s93, 0
	s_add_u32 s34, s92, 0x5000
	s_addc_u32 s35, s93, 0
	s_add_u32 s36, s92, 0x5100
	s_addc_u32 s37, s93, 0
	s_add_u32 s38, s92, 0x5200
	s_addc_u32 s39, s93, 0
	s_add_u32 s40, s92, 0x5300
	s_addc_u32 s41, s93, 0
	s_mov_b32 s49, 1
	v_mov_b32_e32 v16, 0
	s_branch .LBB0_1552

; #define MKCTX() Ctx C; { int t_ = tid_from_wave(wave_s); asm volatile("" : "+v"(t_)); C.lds = (LAS unsigned char*)lds_raw; C.tid = t_; C.lane = t_ & 63; C.wave = __builtin_amdgcn_readfirstlane(t_ >> 6); \
;         C.G = gridDim.x; const int bx_ = blockIdx.x; C.vcu = (C.G % 8 == 0) ? (bx_ % 8) * (C.G / 8) + bx_ / 8 : bx_; C.gw = C.vcu * NWAVES + C.wave; C.NGW = C.G * NWAVES; }
; __global__ void __launch_bounds__(NWAVES * 64, 2) fwd(Args args) {
;     ...
;     if (IN(17)) for (int rep_ = 0; rep_ < NREP(17); ++rep_) { MKCTX();
;         const int P = __builtin_amdgcn_readfirstlane(pexp[272]); const int nfull = (P * 4 / C.G) * C.G;
;         pg8::MoeOrder<4, false> S{C.G, C.vcu, 0, nfull, pexp, 0};
;         pg8::Gemm g{(const bf16*)ACTE, (const bf16*)(ws + WS_WED), 0, 0, FFE / 2};
;         pg8::EpiBf16Plain E{YB, DM, 1.0f / WSC_D}; pg8::gemm_phase<pg8::EpiBf16Plain, pg8::MoeOrder<4, false>, true, true, true>(C.lds, g, S, E, wave_s);
.LBB0_1605:
	s_cmp_lt_i32 s94, 18
	s_cselect_b64 s[0:1], -1, 0
	s_and_b64 s[0:1], s[0:1], s[2:3]
	s_andn2_b64 vcc, exec, s[0:1]
	s_cbranch_vccnz .LBB0_1628
	s_cmp_lt_u32 s96, 0x100
	s_cbranch_scc1 .Lsp_17
	s_setprio 1
.Lsp_17:
	s_waitcnt vmcnt(0)
	v_mbcnt_lo_u32_b32 v0, -1, 0
	v_mbcnt_hi_u32_b32 v0, -1, v0
	v_readlane_b32 s2, v254, 0
	v_add_u32_e32 v0, s96, v0
	v_readlane_b32 s3, v254, 1
	s_load_dword s13, s[2:3], 0x120
	s_mov_b32 s40, s33
	s_waitcnt lgkmcnt(0)
	s_and_b32 s2, s13, 7
	s_cmp_lg_u32 s2, 0
	s_cbranch_scc1 .LBB0_1608
	s_ashr_i32 s2, s33, 31
	s_lshr_b32 s2, s2, 29
	s_add_i32 s2, s33, s2
	s_ashr_i32 s3, s2, 3
	s_and_b32 s2, s2, -8
	s_sub_i32 s2, s33, s2
	s_ashr_i32 s6, s13, 3
	s_mul_i32 s2, s6, s2
	s_add_i32 s40, s2, s3

; __device__ __forceinline__ int tid_from_wave(int wave) { unsigned l_; asm volatile("v_mbcnt_lo_u32_b32 %0, -1, 0\n\tv_mbcnt_hi_u32_b32 %0, -1, %0" : "=v"(l_)); return wave * 64 + (int)l_; }
; __device__ __forceinline__ unsigned xb_ld(unsigned* p)              { return __hip_atomic_load(p, __ATOMIC_RELAXED, __HIP_MEMORY_SCOPE_AGENT); }
; __device__ __forceinline__ unsigned xb_add(unsigned* p, unsigned v) { return __hip_atomic_fetch_add(p, v, __ATOMIC_RELAXED, __HIP_MEMORY_SCOPE_AGENT); }
; __device__ __forceinline__ void xcd_barrier_complete(unsigned* bar, unsigned x, unsigned& nloc, unsigned& nx) {
;     const unsigned G = gridDim.x * gridDim.y * gridDim.z;
;     unsigned sum, cnt, mine, sp = 0u;
;     for (;;) {
;         sum = 0u; cnt = 0u; mine = 0u;
; #pragma unroll
;         for (unsigned j = 0; j < 16; ++j) { const unsigned c = xb_ld(&bar[XB_XCNT(j)]); sum += c; cnt += (c > 0u) ? 1u : 0u; mine = (j == x) ? c : mine; }
;         if (sum == G) break;
; __device__ __forceinline__ void xcd_barrier(const XcdBarrier& b) {
;     asm volatile("s_waitcnt vmcnt(0)" ::: "memory");
;     __syncthreads();
;     if (tid_from_wave(b.wave) == 0) {
;         unsigned* bar = b.bar;
;         __builtin_amdgcn_s_waitcnt(0);
;         unsigned nloc = b.st[0], nx = b.st[1];
;         if (nloc == 0u) { xcd_barrier_complete(bar, b.x, nloc, nx); b.st[0] = nloc; b.st[1] = nx; }
;         const unsigned old = xb_add(&bar[XB_XSUB(b.x)], 1u);
.LBB0_1628:
	s_setprio 0
	s_cmp_gt_i32 s95, 18
	s_cselect_b64 s[2:3], -1, 0
	s_and_b64 s[0:1], s[0:1], s[2:3]
	s_andn2_b64 vcc, exec, s[0:1]
	s_cbranch_vccnz .LBB0_1682
	s_waitcnt vmcnt(0)
	v_readlane_b32 s0, v254, 21
	s_waitcnt vmcnt(0) lgkmcnt(0)
	s_barrier
	v_mbcnt_lo_u32_b32 v0, -1, 0
	v_mbcnt_hi_u32_b32 v0, -1, v0
	s_nop 0
	v_cmp_eq_u32_e32 vcc, s0, v0
	s_and_saveexec_b64 s[0:1], vcc
	s_cbranch_execz .LBB0_1681
	s_add_i32 s6, 0, 0x23d60
	v_mov_b32_e32 v0, s6
	s_waitcnt vmcnt(0) expcnt(0) lgkmcnt(0)
	ds_read_b32 v2, v0
	s_add_i32 s6, 0, 0x23d64
	v_mov_b32_e32 v0, s6
	ds_read_b32 v0, v0
	s_waitcnt lgkmcnt(1)
	v_cmp_ne_u32_e32 vcc, 0, v2
	s_cbranch_vccnz .LBB0_1645
	v_readlane_b32 s6, v254, 0
	v_readlane_b32 s7, v254, 1
	s_load_dwordx2 s[10:11], s[6:7], 0x120
	s_load_dword s9, s[6:7], 0x128
	s_add_u32 s6, s92, 0x4200
	s_addc_u32 s7, s93, 0
	s_add_u32 s8, s92, 0x4400
	s_waitcnt lgkmcnt(0)
	s_mul_i32 s48, s11, s10
	s_mul_i32 s48, s48, s9
	s_addc_u32 s9, s93, 0
	s_add_u32 s10, s92, 0x4500
	s_addc_u32 s11, s93, 0
	s_add_u32 s12, s92, 0x4600
	s_addc_u32 s13, s93, 0
	s_add_u32 s14, s92, 0x4700
	s_addc_u32 s15, s93, 0
	s_add_u32 s16, s92, 0x4800
	s_addc_u32 s17, s93, 0
	s_add_u32 s18, s92, 0x4900
	s_addc_u32 s19, s93, 0
	s_add_u32 s20, s92, 0x4a00
	s_addc_u32 s21, s93, 0
	s_add_u32 s22, s92, 0x4b00
	s_addc_u32 s23, s93, 0
	s_add_u32 s24, s92, 0x4c00
	s_addc_u32 s25, s93, 0
	s_add_u32 s26, s92, 0x4d00
	s_addc_u32 s27, s93, 0
	s_add_u32 s28, s92, 0x4e00
	s_addc_u32 s29, s93, 0
	s_add_u32 s30, s92, 0x4f00
	s_addc_u32 s31, s93, 0
	s_add_u32 s34, s92, 0x5000
	s_addc_u32 s35, s93, 0
	s_add_u32 s36, s92, 0x5100
	s_addc_u32 s37, s93, 0
	s_add_u32 s38, s92, 0x5200
	s_addc_u32 s39, s93, 0
	s_add_u32 s40, s92, 0x5300
	s_addc_u32 s41, s93, 0
	s_mov_b32 s49, 1
	v_mov_b32_e32 v16, 0
	s_branch .LBB0_1633

; #define MKCTX() Ctx C; { int t_ = tid_from_wave(wave_s); asm volatile("" : "+v"(t_)); C.lds = (LAS unsigned char*)lds_raw; C.tid = t_; C.lane = t_ & 63; C.wave = __builtin_amdgcn_readfirstlane(t_ >> 6); \
;         C.G = gridDim.x; const int bx_ = blockIdx.x; C.vcu = (C.G % 8 == 0) ? (bx_ % 8) * (C.G / 8) + bx_ / 8 : bx_; C.gw = C.vcu * NWAVES + C.wave; C.NGW = C.G * NWAVES; }
; __global__ void __launch_bounds__(NWAVES * 64, 2) fwd(Args args) {
;     ...
;     if (IN(18)) { MKCTX();
;         const int P = __builtin_amdgcn_readfirstlane(pexp[272]); const int nfull = (P * 4 / C.G) * C.G, nleft = P * 4 - nfull;
;         if (C.vcu < nleft) {
;             pg8::MoeOrder<4, false> S{C.G, C.vcu, 0, P * 4, pexp, nfull};
.LBB0_1682:
	s_cmp_lt_i32 s94, 19
	s_cselect_b64 s[0:1], -1, 0
	s_and_b64 s[0:1], s[0:1], s[2:3]
	s_andn2_b64 vcc, exec, s[0:1]
	s_cbranch_vccnz .LBB0_1725
	s_cmp_lt_u32 s96, 0x100
	s_cbranch_scc1 .Lsp_18
	s_setprio 1
.Lsp_18:
	v_readlane_b32 s2, v254, 0
	s_waitcnt vmcnt(0)
	v_mbcnt_lo_u32_b32 v0, -1, 0
	v_mbcnt_hi_u32_b32 v0, -1, v0
	v_readlane_b32 s3, v254, 1
	v_add_u32_e32 v4, s96, v0
	s_load_dword s40, s[2:3], 0x120
	v_readfirstlane_b32 s6, v4
	s_mov_b32 s30, s33
	s_waitcnt lgkmcnt(0)
	s_and_b32 s2, s40, 7
	s_cmp_lg_u32 s2, 0
	s_cbranch_scc1 .LBB0_1685
	s_ashr_i32 s3, s33, 31
	s_lshr_b32 s3, s3, 29
	s_add_i32 s3, s33, s3
	s_ashr_i32 s7, s3, 3
	s_and_b32 s3, s3, -8
	s_ashr_i32 s2, s40, 3
	s_sub_i32 s3, s33, s3
	s_mul_i32 s2, s2, s3
	s_add_i32 s30, s2, s7

; __device__ __forceinline__ int tid_from_wave(int wave) { unsigned l_; asm volatile("v_mbcnt_lo_u32_b32 %0, -1, 0\n\tv_mbcnt_hi_u32_b32 %0, -1, %0" : "=v"(l_)); return wave * 64 + (int)l_; }
; __device__ __forceinline__ unsigned xb_ld(unsigned* p)              { return __hip_atomic_load(p, __ATOMIC_RELAXED, __HIP_MEMORY_SCOPE_AGENT); }
; __device__ __forceinline__ unsigned xb_add(unsigned* p, unsigned v) { return __hip_atomic_fetch_add(p, v, __ATOMIC_RELAXED, __HIP_MEMORY_SCOPE_AGENT); }
; __device__ __forceinline__ void xcd_barrier_complete(unsigned* bar, unsigned x, unsigned& nloc, unsigned& nx) {
;     const unsigned G = gridDim.x * gridDim.y * gridDim.z;
;     unsigned sum, cnt, mine, sp = 0u;
;     for (;;) {
;         sum = 0u; cnt = 0u; mine = 0u;
; #pragma unroll
;         for (unsigned j = 0; j < 16; ++j) { const unsigned c = xb_ld(&bar[XB_XCNT(j)]); sum += c; cnt += (c > 0u) ? 1u : 0u; mine = (j == x) ? c : mine; }
;         if (sum == G) break;
; __device__ __forceinline__ void xcd_barrier(const XcdBarrier& b) {
;     asm volatile("s_waitcnt vmcnt(0)" ::: "memory");
;     __syncthreads();
;     if (tid_from_wave(b.wave) == 0) {
;         unsigned* bar = b.bar;
;         __builtin_amdgcn_s_waitcnt(0);
;         unsigned nloc = b.st[0], nx = b.st[1];
;         if (nloc == 0u) { xcd_barrier_complete(bar, b.x, nloc, nx); b.st[0] = nloc; b.st[1] = nx; }
;         const unsigned old = xb_add(&bar[XB_XSUB(b.x)], 1u);
.LBB0_1725:
	s_setprio 0
	s_cmp_gt_i32 s95, 19
	s_cselect_b64 s[2:3], -1, 0
	s_and_b64 s[0:1], s[0:1], s[2:3]
	s_andn2_b64 vcc, exec, s[0:1]
	s_cbranch_vccnz .LBB0_1779
	s_waitcnt vmcnt(0)
	v_readlane_b32 s0, v254, 21
	s_waitcnt vmcnt(0) lgkmcnt(0)
	s_barrier
	v_mbcnt_lo_u32_b32 v0, -1, 0
	v_mbcnt_hi_u32_b32 v0, -1, v0
	s_nop 0
	v_cmp_eq_u32_e32 vcc, s0, v0
	s_and_saveexec_b64 s[0:1], vcc
	s_cbranch_execz .LBB0_1778
	s_add_i32 s4, 0, 0x23d60
	v_mov_b32_e32 v0, s4
	s_waitcnt vmcnt(0) expcnt(0) lgkmcnt(0)
	ds_read_b32 v2, v0
	s_add_i32 s4, 0, 0x23d64
	v_mov_b32_e32 v0, s4
	ds_read_b32 v0, v0
	s_waitcnt lgkmcnt(1)
	v_cmp_ne_u32_e32 vcc, 0, v2
	s_cbranch_vccnz .LBB0_1742
	v_readlane_b32 s4, v254, 0
	v_readlane_b32 s5, v254, 1
	s_load_dwordx2 s[8:9], s[4:5], 0x120
	s_load_dword s7, s[4:5], 0x128
	s_add_u32 s4, s92, 0x4200
	s_addc_u32 s5, s93, 0
	s_add_u32 s6, s92, 0x4400
	s_waitcnt lgkmcnt(0)
	s_mul_i32 s46, s9, s8
	s_mul_i32 s46, s46, s7
	s_addc_u32 s7, s93, 0
	s_add_u32 s8, s92, 0x4500
	s_addc_u32 s9, s93, 0
	s_add_u32 s10, s92, 0x4600
	s_addc_u32 s11, s93, 0
	s_add_u32 s12, s92, 0x4700
	s_addc_u32 s13, s93, 0
	s_add_u32 s14, s92, 0x4800
	s_addc_u32 s15, s93, 0
	s_add_u32 s16, s92, 0x4900
	s_addc_u32 s17, s93, 0
	s_add_u32 s18, s92, 0x4a00
	s_addc_u32 s19, s93, 0
	s_add_u32 s20, s92, 0x4b00
	s_addc_u32 s21, s93, 0
	s_add_u32 s22, s92, 0x4c00
	s_addc_u32 s23, s93, 0
	s_add_u32 s24, s92, 0x4d00
	s_addc_u32 s25, s93, 0
	s_add_u32 s26, s92, 0x4e00
	s_addc_u32 s27, s93, 0
	s_add_u32 s28, s92, 0x4f00
	s_addc_u32 s29, s93, 0
	s_add_u32 s30, s92, 0x5000
	s_addc_u32 s31, s93, 0
	s_add_u32 s34, s92, 0x5100
	s_addc_u32 s35, s93, 0
	s_add_u32 s36, s92, 0x5200
	s_addc_u32 s37, s93, 0
	s_add_u32 s38, s92, 0x5300
	s_addc_u32 s39, s93, 0
	s_mov_b32 s47, 1
	v_mov_b32_e32 v16, 0
	s_branch .LBB0_1730
